# K-loops: t+3 stages use instruction offset:128 (M0 lowered by 128) instead of a 64-bit VALU address add per LDS-DMA (54 adds removed)
# baseline (speedup 1.0000x reference)
; #define PG8_STAGE(bufoff, gbase, voff) do { _Pragma("unroll") for (int _i = 0; _i < 2; ++_i) \
;         __builtin_amdgcn_global_load_lds((const unsigned*)((const char*)(gbase) + (voff)[_i]), (PG8_LAS unsigned*)(lds + (bufoff) + ldsw + _i * 8192), 16, 0, 0); } while (0)
; #define PG8_LDA(dst, b, h) do { _Pragma("unroll") for (int m = 0; m < 4; ++m) { const bf16x8 f0_ = *(const PG8_LAS bf16x8*)(lds + PG8_SA(b, h) + aoff + m * 2048), f1_ = *(const PG8_LAS bf16x8*)(lds + PG8_SA(b, h) + aoff + m * 2048 + 1024); dst[m].set(f0_, f1_); } } while (0)
; #define PG8_LDB(dst, b, h) do { _Pragma("unroll") for (int n = 0; n < 2; ++n) { const bf16x8 f0_ = *(const PG8_LAS bf16x8*)(lds + PG8_SB(b, h) + boff + n * 2048), f1_ = *(const PG8_LAS bf16x8*)(lds + PG8_SB(b, h) + boff + n * 2048 + 1024); dst[n].set(f0_, f1_); } } while (0)
; #define PG8_WAIT_V(n) asm volatile("s_waitcnt vmcnt(" #n ")" ::: "memory")
; #define PG8_WAIT_L(n) asm volatile("s_waitcnt lgkmcnt(" #n ")" ::: "memory")
; #define PG8_BAR __builtin_amdgcn_s_barrier()
; #define PG8_SCHED __builtin_amdgcn_sched_barrier(0)
; template <class Epi, class Sched, bool ALIGN_EPI = false, bool SP2 = false>
; __device__ __forceinline__ void gemm_phase(PG8_LAS unsigned char* lds, const Gemm g, const Sched& S, const Epi& E) {
;     ...
;             const bool last = (t == nt - 2);
;             const char* a1 = cA + (size_t)(t + 1) * kstep;
;             const char* a2 = last ? nA : cA + (size_t)(t + 2) * kstep; const char* b2 = last ? nB : cB + (size_t)(t + 2) * kstep;
;             const char* a3 = a2 + kstep; const char* b3 = b2 + kstep;
;             if (last && has_next) S.a_ready(nxt);
;             if constexpr (SP2) {
;             PG8_LDB(B0, 0, 0); PG8_LDB(B1, 0, 1); PG8_SCHED; PG8_LDA(At, 0, 0); PG8_STAGE(PG8_SA(1, 1), a1 + hstep, voffA);
;             PG8_WAIT_V(8); PG8_WAIT_L(0); PG8_BAR; PG8_MMA(0, 0, At, B0); PG8_MMA(0, 1, At, B1); PG8_BAR; PG8_SCHED;
;             PG8_LDA(At, 0, 1); PG8_STAGE(PG8_SB(0, 0), b2, voffB); PG8_STAGE(PG8_SB(0, 1), b2 + hstepB, voffB); PG8_STAGE(PG8_SA(0, 0), a2, voffA);
;             PG8_WAIT_V(8); PG8_WAIT_L(0); PG8_BAR; PG8_MMA(1, 0, At, B0); PG8_MMA(1, 1, At, B1); PG8_BAR; PG8_SCHED;
.LBB0_204:
	ds_read_b128 v[18:21], v203
	ds_read_b128 v[22:25], v203 offset:1024
	ds_read_b128 v[26:29], v203 offset:2048
	ds_read_b128 v[30:33], v203 offset:3072
	ds_read_b128 v[2:5], v204
	ds_read_b128 v[6:9], v204 offset:1024
	ds_read_b128 v[10:13], v204 offset:2048
	ds_read_b128 v[14:17], v204 offset:3072
	s_add_i32 s53, s48, 2
	s_add_u32 s0, s2, 0x80
	s_addc_u32 s1, s3, 0
	s_cmp_eq_u32 s71, s48
	s_cselect_b32 s48, s44, s0
	s_cselect_b32 s49, s45, s1
	s_cselect_b32 s51, s47, s52
	s_cselect_b32 s50, s46, s20
	s_cmp_eq_u32 s99, 0
	s_cbranch_scc1 .Lkr0_a
	s_add_i32 m0, s66, 0xffffff80
	s_nop 0
	global_load_lds_dwordx4 v[190:191], off offset:128
	s_add_i32 m0, s67, 0xffffff80
	s_nop 0
	global_load_lds_dwordx4 v[192:193], off offset:128
.Lkr0_a:
	v_lshl_add_u64 v[190:191], s[2:3], 0, v[174:175]
	s_add_i32 m0, s58, 0xc000
	ds_read_b128 v[182:185], v205
	ds_read_b128 v[186:189], v205 offset:1024
	ds_read_b128 v[212:215], v205 offset:2048
	ds_read_b128 v[216:219], v205 offset:3072
	ds_read_b128 v[220:223], v205 offset:4096
	ds_read_b128 v[224:227], v205 offset:5120
	ds_read_b128 v[228:231], v205 offset:6144
	ds_read_b128 v[232:235], v205 offset:7168
	global_load_lds_dwordx4 v[190:191], off
	v_lshl_add_u64 v[190:191], s[2:3], 0, v[176:177]
	s_add_i32 m0, s58, 0xe000
	s_nop 0
	global_load_lds_dwordx4 v[190:191], off
	s_waitcnt vmcnt(8)
	s_waitcnt lgkmcnt(0)
	s_barrier
	s_setprio 1
	s_waitcnt lgkmcnt(0)
	v_mfma_scale_f32_16x16x128_f8f6f4 v[158:161], v[18:25], v[182:189], v[158:161], v206, v207 op_sel_hi:[0,0,0]
	v_mfma_scale_f32_16x16x128_f8f6f4 v[154:157], v[26:33], v[182:189], v[154:157], v206, v207 op_sel_hi:[0,0,0]
	v_mfma_scale_f32_16x16x128_f8f6f4 v[142:145], v[18:25], v[212:219], v[142:145], v206, v207 op_sel_hi:[0,0,0]
	v_mfma_scale_f32_16x16x128_f8f6f4 v[138:141], v[26:33], v[212:219], v[138:141], v206, v207 op_sel_hi:[0,0,0]
	v_mfma_scale_f32_16x16x128_f8f6f4 v[126:129], v[18:25], v[220:227], v[126:129], v206, v207 op_sel_hi:[0,0,0]
	v_mfma_scale_f32_16x16x128_f8f6f4 v[122:125], v[26:33], v[220:227], v[122:125], v206, v207 op_sel_hi:[0,0,0]
	v_mfma_scale_f32_16x16x128_f8f6f4 v[110:113], v[18:25], v[228:235], v[110:113], v206, v207 op_sel_hi:[0,0,0]
	v_mfma_scale_f32_16x16x128_f8f6f4 v[106:109], v[26:33], v[228:235], v[106:109], v206, v207 op_sel_hi:[0,0,0]
	s_setprio 0
	s_setprio 1
	v_mfma_scale_f32_16x16x128_f8f6f4 v[150:153], v[2:9], v[182:189], v[150:153], v206, v207 op_sel_hi:[0,0,0]
	v_mfma_scale_f32_16x16x128_f8f6f4 v[146:149], v[10:17], v[182:189], v[146:149], v206, v207 op_sel_hi:[0,0,0]
	v_mfma_scale_f32_16x16x128_f8f6f4 v[134:137], v[2:9], v[212:219], v[134:137], v206, v207 op_sel_hi:[0,0,0]
	v_mfma_scale_f32_16x16x128_f8f6f4 v[130:133], v[10:17], v[212:219], v[130:133], v206, v207 op_sel_hi:[0,0,0]
	v_mfma_scale_f32_16x16x128_f8f6f4 v[118:121], v[2:9], v[220:227], v[118:121], v206, v207 op_sel_hi:[0,0,0]
	v_mfma_scale_f32_16x16x128_f8f6f4 v[114:117], v[10:17], v[220:227], v[114:117], v206, v207 op_sel_hi:[0,0,0]
	v_mfma_scale_f32_16x16x128_f8f6f4 v[102:105], v[2:9], v[228:235], v[102:105], v206, v207 op_sel_hi:[0,0,0]
	v_mfma_scale_f32_16x16x128_f8f6f4 v[98:101], v[10:17], v[228:235], v[98:101], v206, v207 op_sel_hi:[0,0,0]
	s_setprio 0
	s_barrier
	s_add_i32 s0, s76, s57
	v_lshl_add_u64 v[182:183], s[50:51], 0, v[164:165]
	s_mov_b32 m0, s0
	ds_read_b128 v[212:215], v205 offset:16384
	ds_read_b128 v[216:219], v205 offset:17408
	ds_read_b128 v[220:223], v205 offset:18432
	ds_read_b128 v[224:227], v205 offset:19456
	ds_read_b128 v[228:231], v205 offset:20480
	ds_read_b128 v[232:235], v205 offset:21504
	ds_read_b128 v[236:239], v205 offset:22528
	ds_read_b128 v[240:243], v205 offset:23552
	global_load_lds_dwordx4 v[182:183], off
	s_add_i32 m0, s0, 0x2000
	v_lshl_add_u64 v[184:185], s[50:51], 0, v[168:169]
	s_add_u32 s50, s50, s16
	s_addc_u32 s51, s51, s17
	s_add_i32 s0, s77, s57
	global_load_lds_dwordx4 v[184:185], off
	v_lshl_add_u64 v[186:187], s[50:51], 0, v[164:165]
	s_mov_b32 m0, s0
	v_lshl_add_u64 v[188:189], s[50:51], 0, v[168:169]
	global_load_lds_dwordx4 v[186:187], off
	s_add_i32 m0, s0, 0x2000
	v_lshl_add_u64 v[190:191], s[48:49], 0, v[162:163]
	global_load_lds_dwordx4 v[188:189], off
	v_lshl_add_u64 v[192:193], s[48:49], 0, v[166:167]
	s_waitcnt vmcnt(6)
	s_waitcnt lgkmcnt(0)
	s_barrier
; #define PG8_STAGE(bufoff, gbase, voff) do { _Pragma("unroll") for (int _i = 0; _i < 2; ++_i) \
;         __builtin_amdgcn_global_load_lds((const unsigned*)((const char*)(gbase) + (voff)[_i]), (PG8_LAS unsigned*)(lds + (bufoff) + ldsw + _i * 8192), 16, 0, 0); } while (0)
; #define PG8_LDA(dst, b, h) do { _Pragma("unroll") for (int m = 0; m < 4; ++m) { const bf16x8 f0_ = *(const PG8_LAS bf16x8*)(lds + PG8_SA(b, h) + aoff + m * 2048), f1_ = *(const PG8_LAS bf16x8*)(lds + PG8_SA(b, h) + aoff + m * 2048 + 1024); dst[m].set(f0_, f1_); } } while (0)
; #define PG8_LDB(dst, b, h) do { _Pragma("unroll") for (int n = 0; n < 2; ++n) { const bf16x8 f0_ = *(const PG8_LAS bf16x8*)(lds + PG8_SB(b, h) + boff + n * 2048), f1_ = *(const PG8_LAS bf16x8*)(lds + PG8_SB(b, h) + boff + n * 2048 + 1024); dst[n].set(f0_, f1_); } } while (0)
; #define PG8_WAIT_V(n) asm volatile("s_waitcnt vmcnt(" #n ")" ::: "memory")
; #define PG8_WAIT_L(n) asm volatile("s_waitcnt lgkmcnt(" #n ")" ::: "memory")
; #define PG8_BAR __builtin_amdgcn_s_barrier()
; #define PG8_SCHED __builtin_amdgcn_sched_barrier(0)
; template <class Epi, class Sched, bool ALIGN_EPI = false, bool SP2 = false>
; __device__ __forceinline__ void gemm_phase(PG8_LAS unsigned char* lds, const Gemm g, const Sched& S, const Epi& E) {
;     ...
;             PG8_WAIT_V(8); PG8_WAIT_L(0); PG8_BAR; PG8_MMA(1, 0, At, B0); PG8_MMA(1, 1, At, B1); PG8_BAR; PG8_SCHED;
;             PG8_LDB(B0, 1, 0); PG8_LDB(B1, 1, 1); PG8_SCHED; PG8_LDA(At, 1, 0); PG8_STAGE(PG8_SA(0, 1), a2 + hstep, voffA);
;             PG8_WAIT_V(8); PG8_WAIT_L(0); PG8_BAR; PG8_MMA(0, 0, At, B0); PG8_MMA(0, 1, At, B1); PG8_BAR; PG8_SCHED;
;             PG8_LDA(At, 1, 1); PG8_STAGE(PG8_SB(1, 0), b3, voffB); PG8_STAGE(PG8_SB(1, 1), b3 + hstepB, voffB); PG8_STAGE(PG8_SA(1, 0), a3, voffA);
	s_setprio 1
	s_waitcnt lgkmcnt(0)
	v_mfma_scale_f32_16x16x128_f8f6f4 v[94:97], v[18:25], v[212:219], v[94:97], v206, v207 op_sel_hi:[0,0,0]
	v_mfma_scale_f32_16x16x128_f8f6f4 v[90:93], v[26:33], v[212:219], v[90:93], v206, v207 op_sel_hi:[0,0,0]
	v_mfma_scale_f32_16x16x128_f8f6f4 v[78:81], v[18:25], v[220:227], v[78:81], v206, v207 op_sel_hi:[0,0,0]
	v_mfma_scale_f32_16x16x128_f8f6f4 v[74:77], v[26:33], v[220:227], v[74:77], v206, v207 op_sel_hi:[0,0,0]
	v_mfma_scale_f32_16x16x128_f8f6f4 v[62:65], v[18:25], v[228:235], v[62:65], v206, v207 op_sel_hi:[0,0,0]
	v_mfma_scale_f32_16x16x128_f8f6f4 v[58:61], v[26:33], v[228:235], v[58:61], v206, v207 op_sel_hi:[0,0,0]
	v_mfma_scale_f32_16x16x128_f8f6f4 v[46:49], v[18:25], v[236:243], v[46:49], v206, v207 op_sel_hi:[0,0,0]
	v_mfma_scale_f32_16x16x128_f8f6f4 v[42:45], v[26:33], v[236:243], v[42:45], v206, v207 op_sel_hi:[0,0,0]
	s_setprio 0
	s_setprio 1
	v_mfma_scale_f32_16x16x128_f8f6f4 v[86:89], v[2:9], v[212:219], v[86:89], v206, v207 op_sel_hi:[0,0,0]
	v_mfma_scale_f32_16x16x128_f8f6f4 v[82:85], v[10:17], v[212:219], v[82:85], v206, v207 op_sel_hi:[0,0,0]
	v_mfma_scale_f32_16x16x128_f8f6f4 v[70:73], v[2:9], v[220:227], v[70:73], v206, v207 op_sel_hi:[0,0,0]
	v_mfma_scale_f32_16x16x128_f8f6f4 v[66:69], v[10:17], v[220:227], v[66:69], v206, v207 op_sel_hi:[0,0,0]
	v_mfma_scale_f32_16x16x128_f8f6f4 v[54:57], v[2:9], v[228:235], v[54:57], v206, v207 op_sel_hi:[0,0,0]
	v_mfma_scale_f32_16x16x128_f8f6f4 v[50:53], v[10:17], v[228:235], v[50:53], v206, v207 op_sel_hi:[0,0,0]
	v_mfma_scale_f32_16x16x128_f8f6f4 v[38:41], v[2:9], v[236:243], v[38:41], v206, v207 op_sel_hi:[0,0,0]
	v_mfma_scale_f32_16x16x128_f8f6f4 v[34:37], v[10:17], v[236:243], v[34:37], v206, v207 op_sel_hi:[0,0,0]
	s_setprio 0
	s_barrier
	s_add_i32 s0, 0, 0x18000
	s_add_i32 s1, 0, 0x1c000
	v_add_u32_e32 v14, s0, v194
	v_add_u32_e32 v30, s1, v194
	ds_read_b128 v[2:5], v14
	ds_read_b128 v[6:9], v14 offset:1024
	ds_read_b128 v[10:13], v14 offset:2048
	ds_read_b128 v[14:17], v14 offset:3072
	ds_read_b128 v[18:21], v30
	ds_read_b128 v[22:25], v30 offset:1024
	ds_read_b128 v[26:29], v30 offset:2048
	ds_read_b128 v[30:33], v30 offset:3072
	s_add_u32 s48, s48, s14
	s_addc_u32 s49, s49, s15
	s_mov_b32 m0, s61
	v_lshl_add_u64 v[244:245], s[48:49], 0, v[162:163]
	ds_read_b128 v[212:215], v205 offset:32768
	ds_read_b128 v[216:219], v205 offset:33792
	ds_read_b128 v[220:223], v205 offset:34816
	ds_read_b128 v[224:227], v205 offset:35840
	ds_read_b128 v[228:231], v205 offset:36864
	ds_read_b128 v[232:235], v205 offset:37888
	ds_read_b128 v[236:239], v205 offset:38912
	ds_read_b128 v[240:243], v205 offset:39936
	s_mov_b32 m0, s58
	s_nop 0
	global_load_lds_dwordx4 v[190:191], off
	s_mov_b32 m0, s59
	s_nop 0
	global_load_lds_dwordx4 v[192:193], off
	s_mov_b32 m0, s61
	s_nop 0
	global_load_lds_dwordx4 v[244:245], off
	v_lshl_add_u64 v[244:245], s[48:49], 0, v[166:167]
	s_mov_b32 m0, s63
	s_nop 0
	global_load_lds_dwordx4 v[244:245], off
	s_waitcnt vmcnt(8)
	s_waitcnt lgkmcnt(0)
	s_barrier
	s_setprio 1
	s_waitcnt lgkmcnt(0)
	v_mfma_scale_f32_16x16x128_f8f6f4 v[158:161], v[2:9], v[212:219], v[158:161], v206, v207 op_sel_hi:[0,0,0]
	v_mfma_scale_f32_16x16x128_f8f6f4 v[154:157], v[10:17], v[212:219], v[154:157], v206, v207 op_sel_hi:[0,0,0]
	v_mfma_scale_f32_16x16x128_f8f6f4 v[142:145], v[2:9], v[220:227], v[142:145], v206, v207 op_sel_hi:[0,0,0]
	v_mfma_scale_f32_16x16x128_f8f6f4 v[138:141], v[10:17], v[220:227], v[138:141], v206, v207 op_sel_hi:[0,0,0]
	v_mfma_scale_f32_16x16x128_f8f6f4 v[126:129], v[2:9], v[228:235], v[126:129], v206, v207 op_sel_hi:[0,0,0]
	v_mfma_scale_f32_16x16x128_f8f6f4 v[122:125], v[10:17], v[228:235], v[122:125], v206, v207 op_sel_hi:[0,0,0]
	v_mfma_scale_f32_16x16x128_f8f6f4 v[110:113], v[2:9], v[236:243], v[110:113], v206, v207 op_sel_hi:[0,0,0]
	v_mfma_scale_f32_16x16x128_f8f6f4 v[106:109], v[10:17], v[236:243], v[106:109], v206, v207 op_sel_hi:[0,0,0]
	s_setprio 0
	s_setprio 1
	v_mfma_scale_f32_16x16x128_f8f6f4 v[150:153], v[18:25], v[212:219], v[150:153], v206, v207 op_sel_hi:[0,0,0]
	v_mfma_scale_f32_16x16x128_f8f6f4 v[146:149], v[26:33], v[212:219], v[146:149], v206, v207 op_sel_hi:[0,0,0]
	v_mfma_scale_f32_16x16x128_f8f6f4 v[134:137], v[18:25], v[220:227], v[134:137], v206, v207 op_sel_hi:[0,0,0]
	v_mfma_scale_f32_16x16x128_f8f6f4 v[130:133], v[26:33], v[220:227], v[130:133], v206, v207 op_sel_hi:[0,0,0]
	v_mfma_scale_f32_16x16x128_f8f6f4 v[118:121], v[18:25], v[228:235], v[118:121], v206, v207 op_sel_hi:[0,0,0]
	v_mfma_scale_f32_16x16x128_f8f6f4 v[114:117], v[26:33], v[228:235], v[114:117], v206, v207 op_sel_hi:[0,0,0]
	v_mfma_scale_f32_16x16x128_f8f6f4 v[102:105], v[18:25], v[236:243], v[102:105], v206, v207 op_sel_hi:[0,0,0]
	v_mfma_scale_f32_16x16x128_f8f6f4 v[98:101], v[26:33], v[236:243], v[98:101], v206, v207 op_sel_hi:[0,0,0]
	s_setprio 0
	s_barrier
	s_add_i32 s0, s0, s57
	s_add_i32 m0, s0, 0xffffff80
	ds_read_b128 v[212:215], v205 offset:49152
	ds_read_b128 v[216:219], v205 offset:50176
	ds_read_b128 v[220:223], v205 offset:51200
	ds_read_b128 v[224:227], v205 offset:52224
	ds_read_b128 v[228:231], v205 offset:53248
	ds_read_b128 v[232:235], v205 offset:54272
	ds_read_b128 v[236:239], v205 offset:55296
	ds_read_b128 v[240:243], v205 offset:56320
	global_load_lds_dwordx4 v[182:183], off offset:128
	s_add_i32 m0, s0, 0x1f80
	s_add_i32 s0, s1, s57
	global_load_lds_dwordx4 v[184:185], off offset:128
	s_add_i32 m0, s0, 0xffffff80
	s_nop 0
	global_load_lds_dwordx4 v[186:187], off offset:128
	s_add_i32 m0, s0, 0x1f80
	s_nop 0
	global_load_lds_dwordx4 v[188:189], off offset:128
	s_cmp_ge_i32 s53, s69
	s_cbranch_scc0 .Lkr0_b
	s_add_i32 m0, s66, 0xffffff80
	s_nop 0
	global_load_lds_dwordx4 v[190:191], off offset:128
	s_add_i32 m0, s67, 0xffffff80
	s_nop 0
	global_load_lds_dwordx4 v[192:193], off offset:128

; #define PG8_STAGE(bufoff, gbase, voff) do { _Pragma("unroll") for (int _i = 0; _i < 2; ++_i) \
;         __builtin_amdgcn_global_load_lds((const unsigned*)((const char*)(gbase) + (voff)[_i]), (PG8_LAS unsigned*)(lds + (bufoff) + ldsw + _i * 8192), 16, 0, 0); } while (0)
; #define PG8_LDA(dst, b, h) do { _Pragma("unroll") for (int m = 0; m < 4; ++m) { const bf16x8 f0_ = *(const PG8_LAS bf16x8*)(lds + PG8_SA(b, h) + aoff + m * 2048), f1_ = *(const PG8_LAS bf16x8*)(lds + PG8_SA(b, h) + aoff + m * 2048 + 1024); dst[m].set(f0_, f1_); } } while (0)
; #define PG8_LDB(dst, b, h) do { _Pragma("unroll") for (int n = 0; n < 2; ++n) { const bf16x8 f0_ = *(const PG8_LAS bf16x8*)(lds + PG8_SB(b, h) + boff + n * 2048), f1_ = *(const PG8_LAS bf16x8*)(lds + PG8_SB(b, h) + boff + n * 2048 + 1024); dst[n].set(f0_, f1_); } } while (0)
; #define PG8_WAIT_V(n) asm volatile("s_waitcnt vmcnt(" #n ")" ::: "memory")
; #define PG8_WAIT_L(n) asm volatile("s_waitcnt lgkmcnt(" #n ")" ::: "memory")
; #define PG8_BAR __builtin_amdgcn_s_barrier()
; #define PG8_SCHED __builtin_amdgcn_sched_barrier(0)
; template <class Epi, class Sched, bool ALIGN_EPI = false, bool SP2 = false>
; __device__ __forceinline__ void gemm_phase(PG8_LAS unsigned char* lds, const Gemm g, const Sched& S, const Epi& E) {
;     ...
;             const bool last = (t == nt - 2);
;             const char* a1 = cA + (size_t)(t + 1) * kstep;
;             const char* a2 = last ? nA : cA + (size_t)(t + 2) * kstep; const char* b2 = last ? nB : cB + (size_t)(t + 2) * kstep;
;             const char* a3 = a2 + kstep; const char* b3 = b2 + kstep;
;             if (last && has_next) S.a_ready(nxt);
;             if constexpr (SP2) {
;             PG8_LDB(B0, 0, 0); PG8_LDB(B1, 0, 1); PG8_SCHED; PG8_LDA(At, 0, 0); PG8_STAGE(PG8_SA(1, 1), a1 + hstep, voffA);
;             PG8_WAIT_V(8); PG8_WAIT_L(0); PG8_BAR; PG8_MMA(0, 0, At, B0); PG8_MMA(0, 1, At, B1); PG8_BAR; PG8_SCHED;
;             PG8_LDA(At, 0, 1); PG8_STAGE(PG8_SB(0, 0), b2, voffB); PG8_STAGE(PG8_SB(0, 1), b2 + hstepB, voffB); PG8_STAGE(PG8_SA(0, 0), a2, voffA);
;             PG8_WAIT_V(8); PG8_WAIT_L(0); PG8_BAR; PG8_MMA(1, 0, At, B0); PG8_MMA(1, 1, At, B1); PG8_BAR; PG8_SCHED;
.LBB0_984:
	s_add_i32 s75, s42, 2
	v_add_u32_e32 v186, s59, v173
	v_add_u32_e32 v202, s61, v173
	s_add_u32 s0, s38, s40
	ds_read_b128 v[168:171], v186
	ds_read_b128 v[178:181], v186 offset:1024
	ds_read_b128 v[182:185], v186 offset:2048
	ds_read_b128 v[186:189], v186 offset:3072
	ds_read_b128 v[190:193], v202
	ds_read_b128 v[194:197], v202 offset:1024
	ds_read_b128 v[198:201], v202 offset:2048
	ds_read_b128 v[202:205], v202 offset:3072
	s_addc_u32 s1, s39, s41
	s_add_u32 s0, s0, 0x100
	s_addc_u32 s1, s1, 0
	s_add_u32 s33, s73, s40
	s_addc_u32 s76, s74, s41
	s_cmp_eq_u32 s57, s42
	s_cselect_b32 s43, s3, s1
	s_cselect_b32 s42, s2, s0
	s_cselect_b32 s1, s37, s76
	s_cselect_b32 s0, s36, s33
	v_lshl_add_u64 v[240:241], v[164:165], 0, s[40:41]
	s_add_i32 m0, s47, 0xc000
	ds_read_b128 v[206:209], v176
	ds_read_b128 v[212:215], v176 offset:1024
	ds_read_b128 v[216:219], v176 offset:2048
	ds_read_b128 v[220:223], v176 offset:3072
	ds_read_b128 v[224:227], v176 offset:4096
	ds_read_b128 v[228:231], v176 offset:5120
	ds_read_b128 v[232:235], v176 offset:6144
	ds_read_b128 v[236:239], v176 offset:7168
	global_load_lds_dwordx4 v[240:241], off
	v_lshl_add_u64 v[240:241], v[166:167], 0, s[40:41]
	s_add_i32 m0, s47, 0xe000
	s_nop 0
	global_load_lds_dwordx4 v[240:241], off
	s_waitcnt vmcnt(8)
	s_waitcnt lgkmcnt(0)
	s_barrier
	s_setprio 1
	s_waitcnt lgkmcnt(0)
	v_mfma_f32_16x16x32_bf16 v[126:129], v[168:171], v[206:209], v[126:129]
	v_mfma_f32_16x16x32_bf16 v[122:125], v[182:185], v[206:209], v[122:125]
	v_mfma_f32_16x16x32_bf16 v[110:113], v[168:171], v[216:219], v[110:113]
	v_mfma_f32_16x16x32_bf16 v[106:109], v[182:185], v[216:219], v[106:109]
	v_mfma_f32_16x16x32_bf16 v[94:97], v[168:171], v[224:227], v[94:97]
	v_mfma_f32_16x16x32_bf16 v[90:93], v[182:185], v[224:227], v[90:93]
	v_mfma_f32_16x16x32_bf16 v[78:81], v[168:171], v[232:235], v[78:81]
	v_mfma_f32_16x16x32_bf16 v[74:77], v[182:185], v[232:235], v[74:77]
	v_mfma_f32_16x16x32_bf16 v[126:129], v[178:181], v[212:215], v[126:129]
	v_mfma_f32_16x16x32_bf16 v[122:125], v[186:189], v[212:215], v[122:125]
	v_mfma_f32_16x16x32_bf16 v[110:113], v[178:181], v[220:223], v[110:113]
	v_mfma_f32_16x16x32_bf16 v[106:109], v[186:189], v[220:223], v[106:109]
	v_mfma_f32_16x16x32_bf16 v[94:97], v[178:181], v[228:231], v[94:97]
	v_mfma_f32_16x16x32_bf16 v[90:93], v[186:189], v[228:231], v[90:93]
	v_mfma_f32_16x16x32_bf16 v[78:81], v[178:181], v[236:239], v[78:81]
	v_mfma_f32_16x16x32_bf16 v[74:77], v[186:189], v[236:239], v[74:77]
	s_setprio 0
	s_setprio 1
	v_mfma_f32_16x16x32_bf16 v[118:121], v[190:193], v[206:209], v[118:121]
	v_mfma_f32_16x16x32_bf16 v[114:117], v[198:201], v[206:209], v[114:117]
	v_mfma_f32_16x16x32_bf16 v[102:105], v[190:193], v[216:219], v[102:105]
	v_mfma_f32_16x16x32_bf16 v[98:101], v[198:201], v[216:219], v[98:101]
	v_mfma_f32_16x16x32_bf16 v[86:89], v[190:193], v[224:227], v[86:89]
	v_mfma_f32_16x16x32_bf16 v[82:85], v[198:201], v[224:227], v[82:85]
	v_mfma_f32_16x16x32_bf16 v[70:73], v[190:193], v[232:235], v[70:73]
	v_mfma_f32_16x16x32_bf16 v[66:69], v[198:201], v[232:235], v[66:69]
	v_mfma_f32_16x16x32_bf16 v[118:121], v[194:197], v[212:215], v[118:121]
	v_mfma_f32_16x16x32_bf16 v[114:117], v[202:205], v[212:215], v[114:117]
	v_mfma_f32_16x16x32_bf16 v[102:105], v[194:197], v[220:223], v[102:105]
	v_mfma_f32_16x16x32_bf16 v[98:101], v[202:205], v[220:223], v[98:101]
	v_mfma_f32_16x16x32_bf16 v[86:89], v[194:197], v[228:231], v[86:89]
	v_mfma_f32_16x16x32_bf16 v[82:85], v[202:205], v[228:231], v[82:85]
	v_mfma_f32_16x16x32_bf16 v[70:73], v[194:197], v[236:239], v[70:73]
	v_mfma_f32_16x16x32_bf16 v[66:69], v[202:205], v[236:239], v[66:69]
	s_setprio 0
	s_barrier
	s_add_i32 s33, s59, s46
	v_lshl_add_u64 v[240:241], s[0:1], 0, v[132:133]
	s_mov_b32 m0, s33
	ds_read_b128 v[206:209], v176 offset:16384
	ds_read_b128 v[212:215], v176 offset:17408
	ds_read_b128 v[216:219], v176 offset:18432
	ds_read_b128 v[220:223], v176 offset:19456
	ds_read_b128 v[224:227], v176 offset:20480
	ds_read_b128 v[228:231], v176 offset:21504
	ds_read_b128 v[232:235], v176 offset:22528
	ds_read_b128 v[236:239], v176 offset:23552
	global_load_lds_dwordx4 v[240:241], off
	s_add_i32 m0, s33, 0x2000
	v_lshl_add_u64 v[242:243], s[0:1], 0, v[136:137]
	s_add_u32 s0, s0, s14
	s_addc_u32 s1, s1, s15
	s_add_i32 s33, s61, s46
	global_load_lds_dwordx4 v[242:243], off
	v_lshl_add_u64 v[244:245], s[0:1], 0, v[132:133]
	s_mov_b32 m0, s33
	v_lshl_add_u64 v[246:247], s[0:1], 0, v[136:137]
	global_load_lds_dwordx4 v[244:245], off
	s_add_i32 m0, s33, 0x2000
	v_lshl_add_u64 v[248:249], s[42:43], 0, v[130:131]
	global_load_lds_dwordx4 v[246:247], off
	v_lshl_add_u64 v[250:251], s[42:43], 0, v[134:135]
	s_waitcnt vmcnt(6)
	s_waitcnt lgkmcnt(0)
	s_barrier
; #define PG8_STAGE(bufoff, gbase, voff) do { _Pragma("unroll") for (int _i = 0; _i < 2; ++_i) \
;         __builtin_amdgcn_global_load_lds((const unsigned*)((const char*)(gbase) + (voff)[_i]), (PG8_LAS unsigned*)(lds + (bufoff) + ldsw + _i * 8192), 16, 0, 0); } while (0)
; #define PG8_LDA(dst, b, h) do { _Pragma("unroll") for (int m = 0; m < 4; ++m) { const bf16x8 f0_ = *(const PG8_LAS bf16x8*)(lds + PG8_SA(b, h) + aoff + m * 2048), f1_ = *(const PG8_LAS bf16x8*)(lds + PG8_SA(b, h) + aoff + m * 2048 + 1024); dst[m].set(f0_, f1_); } } while (0)
; #define PG8_LDB(dst, b, h) do { _Pragma("unroll") for (int n = 0; n < 2; ++n) { const bf16x8 f0_ = *(const PG8_LAS bf16x8*)(lds + PG8_SB(b, h) + boff + n * 2048), f1_ = *(const PG8_LAS bf16x8*)(lds + PG8_SB(b, h) + boff + n * 2048 + 1024); dst[n].set(f0_, f1_); } } while (0)
; #define PG8_WAIT_V(n) asm volatile("s_waitcnt vmcnt(" #n ")" ::: "memory")
; #define PG8_WAIT_L(n) asm volatile("s_waitcnt lgkmcnt(" #n ")" ::: "memory")
; #define PG8_BAR __builtin_amdgcn_s_barrier()
; #define PG8_SCHED __builtin_amdgcn_sched_barrier(0)
; template <class Epi, class Sched, bool ALIGN_EPI = false, bool SP2 = false>
; __device__ __forceinline__ void gemm_phase(PG8_LAS unsigned char* lds, const Gemm g, const Sched& S, const Epi& E) {
;     ...
;             PG8_WAIT_V(8); PG8_WAIT_L(0); PG8_BAR; PG8_MMA(1, 0, At, B0); PG8_MMA(1, 1, At, B1); PG8_BAR; PG8_SCHED;
;             PG8_LDB(B0, 1, 0); PG8_LDB(B1, 1, 1); PG8_SCHED; PG8_LDA(At, 1, 0); PG8_STAGE(PG8_SA(0, 1), a2 + hstep, voffA);
;             PG8_WAIT_V(8); PG8_WAIT_L(0); PG8_BAR; PG8_MMA(0, 0, At, B0); PG8_MMA(0, 1, At, B1); PG8_BAR; PG8_SCHED;
	s_setprio 1
	s_waitcnt lgkmcnt(0)
	v_mfma_f32_16x16x32_bf16 v[62:65], v[168:171], v[206:209], v[62:65]
	v_mfma_f32_16x16x32_bf16 v[58:61], v[182:185], v[206:209], v[58:61]
	v_mfma_f32_16x16x32_bf16 v[46:49], v[168:171], v[216:219], v[46:49]
	v_mfma_f32_16x16x32_bf16 v[42:45], v[182:185], v[216:219], v[42:45]
	v_mfma_f32_16x16x32_bf16 v[30:33], v[168:171], v[224:227], v[30:33]
	v_mfma_f32_16x16x32_bf16 v[26:29], v[182:185], v[224:227], v[26:29]
	v_mfma_f32_16x16x32_bf16 v[14:17], v[168:171], v[232:235], v[14:17]
	v_mfma_f32_16x16x32_bf16 v[10:13], v[182:185], v[232:235], v[10:13]
	v_mfma_f32_16x16x32_bf16 v[62:65], v[178:181], v[212:215], v[62:65]
	v_mfma_f32_16x16x32_bf16 v[58:61], v[186:189], v[212:215], v[58:61]
	v_mfma_f32_16x16x32_bf16 v[46:49], v[178:181], v[220:223], v[46:49]
	v_mfma_f32_16x16x32_bf16 v[42:45], v[186:189], v[220:223], v[42:45]
	v_mfma_f32_16x16x32_bf16 v[30:33], v[178:181], v[228:231], v[30:33]
	v_mfma_f32_16x16x32_bf16 v[26:29], v[186:189], v[228:231], v[26:29]
	v_mfma_f32_16x16x32_bf16 v[14:17], v[178:181], v[236:239], v[14:17]
	v_mfma_f32_16x16x32_bf16 v[10:13], v[186:189], v[236:239], v[10:13]
	s_setprio 0
	s_setprio 1
	v_mfma_f32_16x16x32_bf16 v[54:57], v[190:193], v[206:209], v[54:57]
	v_mfma_f32_16x16x32_bf16 v[50:53], v[198:201], v[206:209], v[50:53]
	v_mfma_f32_16x16x32_bf16 v[38:41], v[190:193], v[216:219], v[38:41]
	v_mfma_f32_16x16x32_bf16 v[34:37], v[198:201], v[216:219], v[34:37]
	v_mfma_f32_16x16x32_bf16 v[22:25], v[190:193], v[224:227], v[22:25]
	v_mfma_f32_16x16x32_bf16 v[18:21], v[198:201], v[224:227], v[18:21]
	v_mfma_f32_16x16x32_bf16 v[6:9], v[190:193], v[232:235], v[6:9]
	v_mfma_f32_16x16x32_bf16 v[2:5], v[198:201], v[232:235], v[2:5]
	v_mfma_f32_16x16x32_bf16 v[54:57], v[194:197], v[212:215], v[54:57]
	v_mfma_f32_16x16x32_bf16 v[50:53], v[202:205], v[212:215], v[50:53]
	v_mfma_f32_16x16x32_bf16 v[38:41], v[194:197], v[220:223], v[38:41]
	v_mfma_f32_16x16x32_bf16 v[34:37], v[202:205], v[220:223], v[34:37]
	v_mfma_f32_16x16x32_bf16 v[22:25], v[194:197], v[228:231], v[22:25]
	v_mfma_f32_16x16x32_bf16 v[18:21], v[202:205], v[228:231], v[18:21]
	v_mfma_f32_16x16x32_bf16 v[6:9], v[194:197], v[236:239], v[6:9]
	v_mfma_f32_16x16x32_bf16 v[2:5], v[202:205], v[236:239], v[2:5]
	s_setprio 0
	s_barrier
	s_add_i32 s33, 0, 0x18000
	s_add_i32 s76, 0, 0x1c000
	v_add_u32_e32 v186, s33, v173
	v_add_u32_e32 v202, s76, v173
	ds_read_b128 v[168:171], v186
	ds_read_b128 v[178:181], v186 offset:1024
	ds_read_b128 v[182:185], v186 offset:2048
	ds_read_b128 v[186:189], v186 offset:3072
	ds_read_b128 v[190:193], v202
	ds_read_b128 v[194:197], v202 offset:1024
	ds_read_b128 v[198:201], v202 offset:2048
	ds_read_b128 v[202:205], v202 offset:3072
	s_add_u32 s0, s42, s12
	s_addc_u32 s1, s43, s13
	s_mov_b32 m0, s49
	v_lshl_add_u64 v[252:253], s[0:1], 0, v[130:131]
	ds_read_b128 v[206:209], v176 offset:32768
	ds_read_b128 v[212:215], v176 offset:33792
	ds_read_b128 v[216:219], v176 offset:34816
	ds_read_b128 v[220:223], v176 offset:35840
	ds_read_b128 v[224:227], v176 offset:36864
	ds_read_b128 v[228:231], v176 offset:37888
	ds_read_b128 v[232:235], v176 offset:38912
	ds_read_b128 v[236:239], v176 offset:39936
	s_mov_b32 m0, s47
	s_nop 0
	global_load_lds_dwordx4 v[248:249], off
	s_mov_b32 m0, s48
	s_nop 0
	global_load_lds_dwordx4 v[250:251], off
	s_mov_b32 m0, s49
	s_nop 0
	global_load_lds_dwordx4 v[252:253], off
	v_lshl_add_u64 v[252:253], s[0:1], 0, v[134:135]
	s_mov_b32 m0, s50
	s_nop 0
	global_load_lds_dwordx4 v[252:253], off
	s_waitcnt vmcnt(8)
	s_waitcnt lgkmcnt(0)
	s_barrier
; #define PG8_STAGE(bufoff, gbase, voff) do { _Pragma("unroll") for (int _i = 0; _i < 2; ++_i) \
;         __builtin_amdgcn_global_load_lds((const unsigned*)((const char*)(gbase) + (voff)[_i]), (PG8_LAS unsigned*)(lds + (bufoff) + ldsw + _i * 8192), 16, 0, 0); } while (0)
; #define PG8_LDA(dst, b, h) do { _Pragma("unroll") for (int m = 0; m < 4; ++m) { const bf16x8 f0_ = *(const PG8_LAS bf16x8*)(lds + PG8_SA(b, h) + aoff + m * 2048), f1_ = *(const PG8_LAS bf16x8*)(lds + PG8_SA(b, h) + aoff + m * 2048 + 1024); dst[m].set(f0_, f1_); } } while (0)
; #define PG8_WAIT_V(n) asm volatile("s_waitcnt vmcnt(" #n ")" ::: "memory")
; #define PG8_WAIT_L(n) asm volatile("s_waitcnt lgkmcnt(" #n ")" ::: "memory")
; #define PG8_BAR __builtin_amdgcn_s_barrier()
; #define PG8_SCHED __builtin_amdgcn_sched_barrier(0)
; template <class Epi, class Sched, bool ALIGN_EPI = false, bool SP2 = false>
; __device__ __forceinline__ void gemm_phase(PG8_LAS unsigned char* lds, const Gemm g, const Sched& S, const Epi& E) {
;     ...
;             PG8_WAIT_V(8); PG8_WAIT_L(0); PG8_BAR; PG8_MMA(0, 0, At, B0); PG8_MMA(0, 1, At, B1); PG8_BAR; PG8_SCHED;
;             PG8_LDA(At, 1, 1); PG8_STAGE(PG8_SB(1, 0), b3, voffB); PG8_STAGE(PG8_SB(1, 1), b3 + hstepB, voffB); PG8_STAGE(PG8_SA(1, 0), a3, voffA);
;             PG8_WAIT_V(8); PG8_WAIT_L(0); PG8_BAR; PG8_MMA(1, 0, At, B0); PG8_MMA(1, 1, At, B1); PG8_BAR; PG8_SCHED;
	s_setprio 1
	s_waitcnt lgkmcnt(0)
	v_mfma_f32_16x16x32_bf16 v[126:129], v[168:171], v[206:209], v[126:129]
	v_mfma_f32_16x16x32_bf16 v[122:125], v[182:185], v[206:209], v[122:125]
	v_mfma_f32_16x16x32_bf16 v[110:113], v[168:171], v[216:219], v[110:113]
	v_mfma_f32_16x16x32_bf16 v[106:109], v[182:185], v[216:219], v[106:109]
	v_mfma_f32_16x16x32_bf16 v[94:97], v[168:171], v[224:227], v[94:97]
	v_mfma_f32_16x16x32_bf16 v[90:93], v[182:185], v[224:227], v[90:93]
	v_mfma_f32_16x16x32_bf16 v[78:81], v[168:171], v[232:235], v[78:81]
	v_mfma_f32_16x16x32_bf16 v[74:77], v[182:185], v[232:235], v[74:77]
	v_mfma_f32_16x16x32_bf16 v[126:129], v[178:181], v[212:215], v[126:129]
	v_mfma_f32_16x16x32_bf16 v[122:125], v[186:189], v[212:215], v[122:125]
	v_mfma_f32_16x16x32_bf16 v[110:113], v[178:181], v[220:223], v[110:113]
	v_mfma_f32_16x16x32_bf16 v[106:109], v[186:189], v[220:223], v[106:109]
	v_mfma_f32_16x16x32_bf16 v[94:97], v[178:181], v[228:231], v[94:97]
	v_mfma_f32_16x16x32_bf16 v[90:93], v[186:189], v[228:231], v[90:93]
	v_mfma_f32_16x16x32_bf16 v[78:81], v[178:181], v[236:239], v[78:81]
	v_mfma_f32_16x16x32_bf16 v[74:77], v[186:189], v[236:239], v[74:77]
	s_setprio 0
	s_setprio 1
	v_mfma_f32_16x16x32_bf16 v[118:121], v[190:193], v[206:209], v[118:121]
	v_mfma_f32_16x16x32_bf16 v[114:117], v[198:201], v[206:209], v[114:117]
	v_mfma_f32_16x16x32_bf16 v[102:105], v[190:193], v[216:219], v[102:105]
	v_mfma_f32_16x16x32_bf16 v[98:101], v[198:201], v[216:219], v[98:101]
	v_mfma_f32_16x16x32_bf16 v[86:89], v[190:193], v[224:227], v[86:89]
	v_mfma_f32_16x16x32_bf16 v[82:85], v[198:201], v[224:227], v[82:85]
	v_mfma_f32_16x16x32_bf16 v[70:73], v[190:193], v[232:235], v[70:73]
	v_mfma_f32_16x16x32_bf16 v[66:69], v[198:201], v[232:235], v[66:69]
	v_mfma_f32_16x16x32_bf16 v[118:121], v[194:197], v[212:215], v[118:121]
	v_mfma_f32_16x16x32_bf16 v[114:117], v[202:205], v[212:215], v[114:117]
	v_mfma_f32_16x16x32_bf16 v[102:105], v[194:197], v[220:223], v[102:105]
	v_mfma_f32_16x16x32_bf16 v[98:101], v[202:205], v[220:223], v[98:101]
	v_mfma_f32_16x16x32_bf16 v[86:89], v[194:197], v[228:231], v[86:89]
	v_mfma_f32_16x16x32_bf16 v[82:85], v[202:205], v[228:231], v[82:85]
	v_mfma_f32_16x16x32_bf16 v[70:73], v[194:197], v[236:239], v[70:73]
	v_mfma_f32_16x16x32_bf16 v[66:69], v[202:205], v[236:239], v[66:69]
	s_setprio 0
	s_barrier
	s_add_i32 s0, s33, s46
	s_add_i32 m0, s0, 0xffffff80
	ds_read_b128 v[206:209], v176 offset:49152
	ds_read_b128 v[212:215], v176 offset:50176
	ds_read_b128 v[216:219], v176 offset:51200
	ds_read_b128 v[220:223], v176 offset:52224
	ds_read_b128 v[224:227], v176 offset:53248
	ds_read_b128 v[228:231], v176 offset:54272
	ds_read_b128 v[232:235], v176 offset:55296
	ds_read_b128 v[236:239], v176 offset:56320
	global_load_lds_dwordx4 v[240:241], off offset:128
	s_add_i32 m0, s0, 0x1f80
	s_add_i32 s0, s76, s46
	global_load_lds_dwordx4 v[242:243], off offset:128
	s_add_i32 m0, s0, 0xffffff80
	s_nop 0
	global_load_lds_dwordx4 v[244:245], off offset:128
	s_add_i32 m0, s0, 0x1f80
	s_nop 0
	global_load_lds_dwordx4 v[246:247], off offset:128
	s_add_i32 m0, s52, 0xffffff80
	s_nop 0
	global_load_lds_dwordx4 v[248:249], off offset:128
	s_add_i32 m0, s53, 0xffffff80
	s_nop 0
	global_load_lds_dwordx4 v[250:251], off offset:128
	s_waitcnt vmcnt(6)
	s_waitcnt lgkmcnt(0)
	s_barrier
	s_setprio 1
	s_waitcnt lgkmcnt(0)
	v_mfma_f32_16x16x32_bf16 v[62:65], v[168:171], v[206:209], v[62:65]
	v_mfma_f32_16x16x32_bf16 v[58:61], v[182:185], v[206:209], v[58:61]
	v_mfma_f32_16x16x32_bf16 v[46:49], v[168:171], v[216:219], v[46:49]
	v_mfma_f32_16x16x32_bf16 v[42:45], v[182:185], v[216:219], v[42:45]
	v_mfma_f32_16x16x32_bf16 v[30:33], v[168:171], v[224:227], v[30:33]
	v_mfma_f32_16x16x32_bf16 v[26:29], v[182:185], v[224:227], v[26:29]
	v_mfma_f32_16x16x32_bf16 v[14:17], v[168:171], v[232:235], v[14:17]
	v_mfma_f32_16x16x32_bf16 v[10:13], v[182:185], v[232:235], v[10:13]
	v_mfma_f32_16x16x32_bf16 v[62:65], v[178:181], v[212:215], v[62:65]
	v_mfma_f32_16x16x32_bf16 v[58:61], v[186:189], v[212:215], v[58:61]
	v_mfma_f32_16x16x32_bf16 v[46:49], v[178:181], v[220:223], v[46:49]
	v_mfma_f32_16x16x32_bf16 v[42:45], v[186:189], v[220:223], v[42:45]
	v_mfma_f32_16x16x32_bf16 v[30:33], v[178:181], v[228:231], v[30:33]
	v_mfma_f32_16x16x32_bf16 v[26:29], v[186:189], v[228:231], v[26:29]
	v_mfma_f32_16x16x32_bf16 v[14:17], v[178:181], v[236:239], v[14:17]
	v_mfma_f32_16x16x32_bf16 v[10:13], v[186:189], v[236:239], v[10:13]
	s_setprio 0
	s_setprio 1
	v_mfma_f32_16x16x32_bf16 v[54:57], v[190:193], v[206:209], v[54:57]
	v_mfma_f32_16x16x32_bf16 v[50:53], v[198:201], v[206:209], v[50:53]
	v_mfma_f32_16x16x32_bf16 v[38:41], v[190:193], v[216:219], v[38:41]
	v_mfma_f32_16x16x32_bf16 v[34:37], v[198:201], v[216:219], v[34:37]
	v_mfma_f32_16x16x32_bf16 v[22:25], v[190:193], v[224:227], v[22:25]
	v_mfma_f32_16x16x32_bf16 v[18:21], v[198:201], v[224:227], v[18:21]
	v_mfma_f32_16x16x32_bf16 v[6:9], v[190:193], v[232:235], v[6:9]
	v_mfma_f32_16x16x32_bf16 v[2:5], v[198:201], v[232:235], v[2:5]
	v_mfma_f32_16x16x32_bf16 v[54:57], v[194:197], v[212:215], v[54:57]
	v_mfma_f32_16x16x32_bf16 v[50:53], v[202:205], v[212:215], v[50:53]
	v_mfma_f32_16x16x32_bf16 v[38:41], v[194:197], v[220:223], v[38:41]
	v_mfma_f32_16x16x32_bf16 v[34:37], v[202:205], v[220:223], v[34:37]
	v_mfma_f32_16x16x32_bf16 v[22:25], v[194:197], v[228:231], v[22:25]
	v_mfma_f32_16x16x32_bf16 v[18:21], v[202:205], v[228:231], v[18:21]
	v_mfma_f32_16x16x32_bf16 v[6:9], v[194:197], v[236:239], v[6:9]
	v_mfma_f32_16x16x32_bf16 v[2:5], v[202:205], v[236:239], v[2:5]
	s_setprio 0
	s_barrier
	s_add_u32 s40, s40, 0x100
	s_addc_u32 s41, s41, 0
	s_cmp_ge_i32 s75, s54
	s_cbranch_scc0 .LBB0_982

; #define PG8_STAGE(bufoff, gbase, voff) do { _Pragma("unroll") for (int _i = 0; _i < 2; ++_i) \
;         __builtin_amdgcn_global_load_lds((const unsigned*)((const char*)(gbase) + (voff)[_i]), (PG8_LAS unsigned*)(lds + (bufoff) + ldsw + _i * 8192), 16, 0, 0); } while (0)
; #define PG8_LDA(dst, b, h) do { _Pragma("unroll") for (int m = 0; m < 4; ++m) { const bf16x8 f0_ = *(const PG8_LAS bf16x8*)(lds + PG8_SA(b, h) + aoff + m * 2048), f1_ = *(const PG8_LAS bf16x8*)(lds + PG8_SA(b, h) + aoff + m * 2048 + 1024); dst[m].set(f0_, f1_); } } while (0)
; #define PG8_LDB(dst, b, h) do { _Pragma("unroll") for (int n = 0; n < 2; ++n) { const bf16x8 f0_ = *(const PG8_LAS bf16x8*)(lds + PG8_SB(b, h) + boff + n * 2048), f1_ = *(const PG8_LAS bf16x8*)(lds + PG8_SB(b, h) + boff + n * 2048 + 1024); dst[n].set(f0_, f1_); } } while (0)
; #define PG8_WAIT_V(n) asm volatile("s_waitcnt vmcnt(" #n ")" ::: "memory")
; #define PG8_WAIT_L(n) asm volatile("s_waitcnt lgkmcnt(" #n ")" ::: "memory")
; #define PG8_BAR __builtin_amdgcn_s_barrier()
; #define PG8_SCHED __builtin_amdgcn_sched_barrier(0)
; template <class Epi, class Sched, bool ALIGN_EPI = false, bool SP2 = false>
; __device__ __forceinline__ void gemm_phase(PG8_LAS unsigned char* lds, const Gemm g, const Sched& S, const Epi& E) {
;     ...
;             const bool last = (t == nt - 2);
;             const char* a1 = cA + (size_t)(t + 1) * kstep;
;             const char* a2 = last ? nA : cA + (size_t)(t + 2) * kstep; const char* b2 = last ? nB : cB + (size_t)(t + 2) * kstep;
;             const char* a3 = a2 + kstep; const char* b3 = b2 + kstep;
;             if (last && has_next) S.a_ready(nxt);
;             if constexpr (SP2) {
;             PG8_LDB(B0, 0, 0); PG8_LDB(B1, 0, 1); PG8_SCHED; PG8_LDA(At, 0, 0); PG8_STAGE(PG8_SA(1, 1), a1 + hstep, voffA);
;             PG8_WAIT_V(8); PG8_WAIT_L(0); PG8_BAR; PG8_MMA(0, 0, At, B0); PG8_MMA(0, 1, At, B1); PG8_BAR; PG8_SCHED;
;             PG8_LDA(At, 0, 1); PG8_STAGE(PG8_SB(0, 0), b2, voffB); PG8_STAGE(PG8_SB(0, 1), b2 + hstepB, voffB); PG8_STAGE(PG8_SA(0, 0), a2, voffA);
;             PG8_WAIT_V(8); PG8_WAIT_L(0); PG8_BAR; PG8_MMA(1, 0, At, B0); PG8_MMA(1, 1, At, B1); PG8_BAR; PG8_SCHED;
.LBB0_1070:
	ds_read_b128 v[130:133], v193
	ds_read_b128 v[134:137], v193 offset:1024
	ds_read_b128 v[138:141], v193 offset:2048
	ds_read_b128 v[142:145], v193 offset:3072
	ds_read_b128 v[146:149], v194
	ds_read_b128 v[150:153], v194 offset:1024
	ds_read_b128 v[154:157], v194 offset:2048
	ds_read_b128 v[158:161], v194 offset:3072
	s_add_i32 s95, s58, 2
	s_add_u32 s0, s56, 0x80
	s_addc_u32 s1, s57, 0
	s_cmp_eq_u32 s78, s58
	s_cselect_b32 s58, s2, s0
	s_cselect_b32 s59, s3, s1
	s_cselect_b32 s1, s55, s94
	s_cselect_b32 s0, s54, s93
	s_cmp_eq_u32 s99, 0
	s_cbranch_scc1 .Lkr2_a
	s_add_i32 m0, s74, 0xffffff80
	s_nop 0
	global_load_lds_dwordx4 v[232:233], off offset:128
	s_add_i32 m0, s75, 0xffffff80
	s_nop 0
	global_load_lds_dwordx4 v[234:235], off offset:128
.Lkr2_a:
	v_lshl_add_u64 v[224:225], s[56:57], 0, v[176:177]
	s_add_i32 m0, s67, 0xc000
	ds_read_b128 v[162:165], v195
	ds_read_b128 v[186:189], v195 offset:1024
	ds_read_b128 v[198:201], v195 offset:2048
	ds_read_b128 v[202:205], v195 offset:3072
	ds_read_b128 v[206:209], v195 offset:4096
	ds_read_b128 v[212:215], v195 offset:5120
	ds_read_b128 v[216:219], v195 offset:6144
	ds_read_b128 v[220:223], v195 offset:7168
	global_load_lds_dwordx4 v[224:225], off
	v_lshl_add_u64 v[224:225], s[56:57], 0, v[178:179]
	s_add_i32 m0, s67, 0xe000
	s_nop 0
	global_load_lds_dwordx4 v[224:225], off
	s_waitcnt vmcnt(8)
	s_waitcnt lgkmcnt(0)
	s_barrier
	s_setprio 1
	s_waitcnt lgkmcnt(0)
	v_mfma_f32_16x16x32_bf16 v[126:129], v[130:133], v[162:165], v[126:129]
	v_mfma_f32_16x16x32_bf16 v[122:125], v[138:141], v[162:165], v[122:125]
	v_mfma_f32_16x16x32_bf16 v[58:61], v[130:133], v[198:201], v[58:61]
	v_mfma_f32_16x16x32_bf16 v[62:65], v[138:141], v[198:201], v[62:65]
	v_mfma_f32_16x16x32_bf16 v[106:109], v[130:133], v[206:209], v[106:109]
	v_mfma_f32_16x16x32_bf16 v[110:113], v[138:141], v[206:209], v[110:113]
	v_mfma_f32_16x16x32_bf16 v[98:101], v[130:133], v[216:219], v[98:101]
	v_mfma_f32_16x16x32_bf16 v[102:105], v[138:141], v[216:219], v[102:105]
	v_mfma_f32_16x16x32_bf16 v[126:129], v[134:137], v[186:189], v[126:129]
	v_mfma_f32_16x16x32_bf16 v[122:125], v[142:145], v[186:189], v[122:125]
	v_mfma_f32_16x16x32_bf16 v[58:61], v[134:137], v[202:205], v[58:61]
	v_mfma_f32_16x16x32_bf16 v[62:65], v[142:145], v[202:205], v[62:65]
	v_mfma_f32_16x16x32_bf16 v[106:109], v[134:137], v[212:215], v[106:109]
	v_mfma_f32_16x16x32_bf16 v[110:113], v[142:145], v[212:215], v[110:113]
	v_mfma_f32_16x16x32_bf16 v[98:101], v[134:137], v[220:223], v[98:101]
	v_mfma_f32_16x16x32_bf16 v[102:105], v[142:145], v[220:223], v[102:105]
	s_setprio 0
	s_setprio 1
	v_mfma_f32_16x16x32_bf16 v[118:121], v[146:149], v[162:165], v[118:121]
	v_mfma_f32_16x16x32_bf16 v[114:117], v[154:157], v[162:165], v[114:117]
	v_mfma_f32_16x16x32_bf16 v[50:53], v[146:149], v[198:201], v[50:53]
	v_mfma_f32_16x16x32_bf16 v[54:57], v[154:157], v[198:201], v[54:57]
	v_mfma_f32_16x16x32_bf16 v[90:93], v[146:149], v[206:209], v[90:93]
	v_mfma_f32_16x16x32_bf16 v[94:97], v[154:157], v[206:209], v[94:97]
	v_mfma_f32_16x16x32_bf16 v[74:77], v[146:149], v[216:219], v[74:77]
	v_mfma_f32_16x16x32_bf16 v[78:81], v[154:157], v[216:219], v[78:81]
	v_mfma_f32_16x16x32_bf16 v[118:121], v[150:153], v[186:189], v[118:121]
	v_mfma_f32_16x16x32_bf16 v[114:117], v[158:161], v[186:189], v[114:117]
	v_mfma_f32_16x16x32_bf16 v[50:53], v[150:153], v[202:205], v[50:53]
	v_mfma_f32_16x16x32_bf16 v[54:57], v[158:161], v[202:205], v[54:57]
	v_mfma_f32_16x16x32_bf16 v[90:93], v[150:153], v[212:215], v[90:93]
	v_mfma_f32_16x16x32_bf16 v[94:97], v[158:161], v[212:215], v[94:97]
	v_mfma_f32_16x16x32_bf16 v[74:77], v[150:153], v[220:223], v[74:77]
	v_mfma_f32_16x16x32_bf16 v[78:81], v[158:161], v[220:223], v[78:81]
	s_setprio 0
	s_barrier
	s_add_i32 s33, s82, s66
	v_lshl_add_u64 v[224:225], s[0:1], 0, v[168:169]
	s_mov_b32 m0, s33
	ds_read_b128 v[162:165], v195 offset:16384
	ds_read_b128 v[186:189], v195 offset:17408
	ds_read_b128 v[198:201], v195 offset:18432
	ds_read_b128 v[202:205], v195 offset:19456
	ds_read_b128 v[206:209], v195 offset:20480
	ds_read_b128 v[212:215], v195 offset:21504
	ds_read_b128 v[216:219], v195 offset:22528
	ds_read_b128 v[220:223], v195 offset:23552
	global_load_lds_dwordx4 v[224:225], off
	s_add_i32 m0, s33, 0x2000
	v_lshl_add_u64 v[226:227], s[0:1], 0, v[172:173]
	s_add_u32 s0, s0, s16
	s_addc_u32 s1, s1, s17
	s_add_i32 s33, s83, s66
	global_load_lds_dwordx4 v[226:227], off
	v_lshl_add_u64 v[228:229], s[0:1], 0, v[168:169]
	s_mov_b32 m0, s33
	v_lshl_add_u64 v[230:231], s[0:1], 0, v[172:173]
	global_load_lds_dwordx4 v[228:229], off
	s_add_i32 m0, s33, 0x2000
	v_lshl_add_u64 v[232:233], s[58:59], 0, v[166:167]
	global_load_lds_dwordx4 v[230:231], off
	v_lshl_add_u64 v[234:235], s[58:59], 0, v[170:171]
	s_waitcnt vmcnt(6)
	s_waitcnt lgkmcnt(0)
	s_barrier
; #define PG8_STAGE(bufoff, gbase, voff) do { _Pragma("unroll") for (int _i = 0; _i < 2; ++_i) \
;         __builtin_amdgcn_global_load_lds((const unsigned*)((const char*)(gbase) + (voff)[_i]), (PG8_LAS unsigned*)(lds + (bufoff) + ldsw + _i * 8192), 16, 0, 0); } while (0)
; #define PG8_LDA(dst, b, h) do { _Pragma("unroll") for (int m = 0; m < 4; ++m) { const bf16x8 f0_ = *(const PG8_LAS bf16x8*)(lds + PG8_SA(b, h) + aoff + m * 2048), f1_ = *(const PG8_LAS bf16x8*)(lds + PG8_SA(b, h) + aoff + m * 2048 + 1024); dst[m].set(f0_, f1_); } } while (0)
; #define PG8_LDB(dst, b, h) do { _Pragma("unroll") for (int n = 0; n < 2; ++n) { const bf16x8 f0_ = *(const PG8_LAS bf16x8*)(lds + PG8_SB(b, h) + boff + n * 2048), f1_ = *(const PG8_LAS bf16x8*)(lds + PG8_SB(b, h) + boff + n * 2048 + 1024); dst[n].set(f0_, f1_); } } while (0)
; #define PG8_WAIT_V(n) asm volatile("s_waitcnt vmcnt(" #n ")" ::: "memory")
; #define PG8_WAIT_L(n) asm volatile("s_waitcnt lgkmcnt(" #n ")" ::: "memory")
; #define PG8_BAR __builtin_amdgcn_s_barrier()
; #define PG8_SCHED __builtin_amdgcn_sched_barrier(0)
; template <class Epi, class Sched, bool ALIGN_EPI = false, bool SP2 = false>
; __device__ __forceinline__ void gemm_phase(PG8_LAS unsigned char* lds, const Gemm g, const Sched& S, const Epi& E) {
;     ...
;             PG8_WAIT_V(8); PG8_WAIT_L(0); PG8_BAR; PG8_MMA(1, 0, At, B0); PG8_MMA(1, 1, At, B1); PG8_BAR; PG8_SCHED;
;             PG8_LDB(B0, 1, 0); PG8_LDB(B1, 1, 1); PG8_SCHED; PG8_LDA(At, 1, 0); PG8_STAGE(PG8_SA(0, 1), a2 + hstep, voffA);
;             PG8_WAIT_V(8); PG8_WAIT_L(0); PG8_BAR; PG8_MMA(0, 0, At, B0); PG8_MMA(0, 1, At, B1); PG8_BAR; PG8_SCHED;
;             PG8_LDA(At, 1, 1); PG8_STAGE(PG8_SB(1, 0), b3, voffB); PG8_STAGE(PG8_SB(1, 1), b3 + hstepB, voffB); PG8_STAGE(PG8_SA(1, 0), a3, voffA);
	s_setprio 1
	s_waitcnt lgkmcnt(0)
	v_mfma_f32_16x16x32_bf16 v[82:85], v[130:133], v[162:165], v[82:85]
	v_mfma_f32_16x16x32_bf16 v[86:89], v[138:141], v[162:165], v[86:89]
	v_mfma_f32_16x16x32_bf16 v[46:49], v[130:133], v[198:201], v[46:49]
	v_mfma_f32_16x16x32_bf16 v[42:45], v[138:141], v[198:201], v[42:45]
	v_mfma_f32_16x16x32_bf16 v[30:33], v[130:133], v[206:209], v[30:33]
	v_mfma_f32_16x16x32_bf16 v[26:29], v[138:141], v[206:209], v[26:29]
	v_mfma_f32_16x16x32_bf16 v[14:17], v[130:133], v[216:219], v[14:17]
	v_mfma_f32_16x16x32_bf16 v[6:9], v[138:141], v[216:219], v[6:9]
	v_mfma_f32_16x16x32_bf16 v[82:85], v[134:137], v[186:189], v[82:85]
	v_mfma_f32_16x16x32_bf16 v[86:89], v[142:145], v[186:189], v[86:89]
	v_mfma_f32_16x16x32_bf16 v[46:49], v[134:137], v[202:205], v[46:49]
	v_mfma_f32_16x16x32_bf16 v[42:45], v[142:145], v[202:205], v[42:45]
	v_mfma_f32_16x16x32_bf16 v[30:33], v[134:137], v[212:215], v[30:33]
	v_mfma_f32_16x16x32_bf16 v[26:29], v[142:145], v[212:215], v[26:29]
	v_mfma_f32_16x16x32_bf16 v[14:17], v[134:137], v[220:223], v[14:17]
	v_mfma_f32_16x16x32_bf16 v[6:9], v[142:145], v[220:223], v[6:9]
	s_setprio 0
	s_setprio 1
	v_mfma_f32_16x16x32_bf16 v[66:69], v[146:149], v[162:165], v[66:69]
	v_mfma_f32_16x16x32_bf16 v[70:73], v[154:157], v[162:165], v[70:73]
	v_mfma_f32_16x16x32_bf16 v[38:41], v[146:149], v[198:201], v[38:41]
	v_mfma_f32_16x16x32_bf16 v[34:37], v[154:157], v[198:201], v[34:37]
	v_mfma_f32_16x16x32_bf16 v[22:25], v[146:149], v[206:209], v[22:25]
	v_mfma_f32_16x16x32_bf16 v[18:21], v[154:157], v[206:209], v[18:21]
	v_mfma_f32_16x16x32_bf16 v[10:13], v[146:149], v[216:219], v[10:13]
	v_mfma_f32_16x16x32_bf16 v[2:5], v[154:157], v[216:219], v[2:5]
	v_mfma_f32_16x16x32_bf16 v[66:69], v[150:153], v[186:189], v[66:69]
	v_mfma_f32_16x16x32_bf16 v[70:73], v[158:161], v[186:189], v[70:73]
	v_mfma_f32_16x16x32_bf16 v[38:41], v[150:153], v[202:205], v[38:41]
	v_mfma_f32_16x16x32_bf16 v[34:37], v[158:161], v[202:205], v[34:37]
	v_mfma_f32_16x16x32_bf16 v[22:25], v[150:153], v[212:215], v[22:25]
	v_mfma_f32_16x16x32_bf16 v[18:21], v[158:161], v[212:215], v[18:21]
	v_mfma_f32_16x16x32_bf16 v[10:13], v[150:153], v[220:223], v[10:13]
	v_mfma_f32_16x16x32_bf16 v[2:5], v[158:161], v[220:223], v[2:5]
	s_setprio 0
	s_barrier
	s_add_i32 s33, 0, 0x18000
	s_add_i32 s96, 0, 0x1c000
	v_add_u32_e32 v142, s33, v190
	v_add_u32_e32 v158, s96, v190
	ds_read_b128 v[130:133], v142
	ds_read_b128 v[134:137], v142 offset:1024
	ds_read_b128 v[138:141], v142 offset:2048
	ds_read_b128 v[142:145], v142 offset:3072
	ds_read_b128 v[146:149], v158
	ds_read_b128 v[150:153], v158 offset:1024
	ds_read_b128 v[154:157], v158 offset:2048
	ds_read_b128 v[158:161], v158 offset:3072
	s_add_u32 s0, s58, s14
	s_addc_u32 s1, s59, s15
	s_mov_b32 m0, s71
	v_lshl_add_u64 v[236:237], s[0:1], 0, v[166:167]
	ds_read_b128 v[162:165], v195 offset:32768
	ds_read_b128 v[186:189], v195 offset:33792
	ds_read_b128 v[198:201], v195 offset:34816
	ds_read_b128 v[202:205], v195 offset:35840
	ds_read_b128 v[206:209], v195 offset:36864
	ds_read_b128 v[212:215], v195 offset:37888
	ds_read_b128 v[216:219], v195 offset:38912
	ds_read_b128 v[220:223], v195 offset:39936
	s_mov_b32 m0, s67
	s_nop 0
	global_load_lds_dwordx4 v[232:233], off
	s_mov_b32 m0, s69
	s_nop 0
	global_load_lds_dwordx4 v[234:235], off
	s_mov_b32 m0, s71
	s_nop 0
	global_load_lds_dwordx4 v[236:237], off
	v_lshl_add_u64 v[236:237], s[0:1], 0, v[170:171]
	s_mov_b32 m0, s73
	s_nop 0
	global_load_lds_dwordx4 v[236:237], off
	s_waitcnt vmcnt(8)
	s_waitcnt lgkmcnt(0)
	s_barrier
	s_setprio 1
	s_waitcnt lgkmcnt(0)
	v_mfma_f32_16x16x32_bf16 v[126:129], v[130:133], v[162:165], v[126:129]
	v_mfma_f32_16x16x32_bf16 v[122:125], v[138:141], v[162:165], v[122:125]
	v_mfma_f32_16x16x32_bf16 v[58:61], v[130:133], v[198:201], v[58:61]
	v_mfma_f32_16x16x32_bf16 v[62:65], v[138:141], v[198:201], v[62:65]
	v_mfma_f32_16x16x32_bf16 v[106:109], v[130:133], v[206:209], v[106:109]
	v_mfma_f32_16x16x32_bf16 v[110:113], v[138:141], v[206:209], v[110:113]
	v_mfma_f32_16x16x32_bf16 v[98:101], v[130:133], v[216:219], v[98:101]
	v_mfma_f32_16x16x32_bf16 v[102:105], v[138:141], v[216:219], v[102:105]
	v_mfma_f32_16x16x32_bf16 v[126:129], v[134:137], v[186:189], v[126:129]
	v_mfma_f32_16x16x32_bf16 v[122:125], v[142:145], v[186:189], v[122:125]
	v_mfma_f32_16x16x32_bf16 v[58:61], v[134:137], v[202:205], v[58:61]
	v_mfma_f32_16x16x32_bf16 v[62:65], v[142:145], v[202:205], v[62:65]
	v_mfma_f32_16x16x32_bf16 v[106:109], v[134:137], v[212:215], v[106:109]
	v_mfma_f32_16x16x32_bf16 v[110:113], v[142:145], v[212:215], v[110:113]
	v_mfma_f32_16x16x32_bf16 v[98:101], v[134:137], v[220:223], v[98:101]
	v_mfma_f32_16x16x32_bf16 v[102:105], v[142:145], v[220:223], v[102:105]
	s_setprio 0
	s_setprio 1
	v_mfma_f32_16x16x32_bf16 v[118:121], v[146:149], v[162:165], v[118:121]
	v_mfma_f32_16x16x32_bf16 v[114:117], v[154:157], v[162:165], v[114:117]
	v_mfma_f32_16x16x32_bf16 v[50:53], v[146:149], v[198:201], v[50:53]
	v_mfma_f32_16x16x32_bf16 v[54:57], v[154:157], v[198:201], v[54:57]
	v_mfma_f32_16x16x32_bf16 v[90:93], v[146:149], v[206:209], v[90:93]
	v_mfma_f32_16x16x32_bf16 v[94:97], v[154:157], v[206:209], v[94:97]
	v_mfma_f32_16x16x32_bf16 v[74:77], v[146:149], v[216:219], v[74:77]
	v_mfma_f32_16x16x32_bf16 v[78:81], v[154:157], v[216:219], v[78:81]
	v_mfma_f32_16x16x32_bf16 v[118:121], v[150:153], v[186:189], v[118:121]
	v_mfma_f32_16x16x32_bf16 v[114:117], v[158:161], v[186:189], v[114:117]
	v_mfma_f32_16x16x32_bf16 v[50:53], v[150:153], v[202:205], v[50:53]
	v_mfma_f32_16x16x32_bf16 v[54:57], v[158:161], v[202:205], v[54:57]
	v_mfma_f32_16x16x32_bf16 v[90:93], v[150:153], v[212:215], v[90:93]
	v_mfma_f32_16x16x32_bf16 v[94:97], v[158:161], v[212:215], v[94:97]
	v_mfma_f32_16x16x32_bf16 v[74:77], v[150:153], v[220:223], v[74:77]
	v_mfma_f32_16x16x32_bf16 v[78:81], v[158:161], v[220:223], v[78:81]
	s_setprio 0
	s_barrier
	s_add_i32 s0, s33, s66
	s_add_i32 m0, s0, 0xffffff80
	ds_read_b128 v[162:165], v195 offset:49152
	ds_read_b128 v[186:189], v195 offset:50176
	ds_read_b128 v[198:201], v195 offset:51200
	ds_read_b128 v[202:205], v195 offset:52224
	ds_read_b128 v[206:209], v195 offset:53248
	ds_read_b128 v[212:215], v195 offset:54272
	ds_read_b128 v[216:219], v195 offset:55296
	ds_read_b128 v[220:223], v195 offset:56320
	global_load_lds_dwordx4 v[224:225], off offset:128
	s_add_i32 m0, s0, 0x1f80
	s_add_i32 s0, s96, s66
	global_load_lds_dwordx4 v[226:227], off offset:128
	s_add_i32 m0, s0, 0xffffff80
	s_nop 0
	global_load_lds_dwordx4 v[228:229], off offset:128
	s_add_i32 m0, s0, 0x1f80
	s_nop 0
	global_load_lds_dwordx4 v[230:231], off offset:128
	s_cmp_ge_i32 s95, s76
	s_cbranch_scc0 .Lkr2_b
	s_add_i32 m0, s74, 0xffffff80
	s_nop 0
	global_load_lds_dwordx4 v[232:233], off offset:128
	s_add_i32 m0, s75, 0xffffff80
	s_nop 0
	global_load_lds_dwordx4 v[234:235], off offset:128

; #define PG8_STAGE(bufoff, gbase, voff) do { _Pragma("unroll") for (int _i = 0; _i < 2; ++_i) \
;         __builtin_amdgcn_global_load_lds((const unsigned*)((const char*)(gbase) + (voff)[_i]), (PG8_LAS unsigned*)(lds + (bufoff) + ldsw + _i * 8192), 16, 0, 0); } while (0)
; #define PG8_LDA(dst, b, h) do { _Pragma("unroll") for (int m = 0; m < 4; ++m) { const bf16x8 f0_ = *(const PG8_LAS bf16x8*)(lds + PG8_SA(b, h) + aoff + m * 2048), f1_ = *(const PG8_LAS bf16x8*)(lds + PG8_SA(b, h) + aoff + m * 2048 + 1024); dst[m].set(f0_, f1_); } } while (0)
; #define PG8_LDB(dst, b, h) do { _Pragma("unroll") for (int n = 0; n < 2; ++n) { const bf16x8 f0_ = *(const PG8_LAS bf16x8*)(lds + PG8_SB(b, h) + boff + n * 2048), f1_ = *(const PG8_LAS bf16x8*)(lds + PG8_SB(b, h) + boff + n * 2048 + 1024); dst[n].set(f0_, f1_); } } while (0)
; #define PG8_WAIT_V(n) asm volatile("s_waitcnt vmcnt(" #n ")" ::: "memory")
; #define PG8_WAIT_L(n) asm volatile("s_waitcnt lgkmcnt(" #n ")" ::: "memory")
; #define PG8_BAR __builtin_amdgcn_s_barrier()
; #define PG8_SCHED __builtin_amdgcn_sched_barrier(0)
; template <class Epi, class Sched, bool ALIGN_EPI = false, bool SP2 = false>
; __device__ __forceinline__ void gemm_phase(PG8_LAS unsigned char* lds, const Gemm g, const Sched& S, const Epi& E) {
;     ...
;             const bool last = (t == nt - 2);
;             const char* a1 = cA + (size_t)(t + 1) * kstep;
;             const char* a2 = last ? nA : cA + (size_t)(t + 2) * kstep; const char* b2 = last ? nB : cB + (size_t)(t + 2) * kstep;
;             const char* a3 = a2 + kstep; const char* b3 = b2 + kstep;
;             if (last && has_next) S.a_ready(nxt);
;             if constexpr (SP2) {
;             PG8_LDB(B0, 0, 0); PG8_LDB(B1, 0, 1); PG8_SCHED; PG8_LDA(At, 0, 0); PG8_STAGE(PG8_SA(1, 1), a1 + hstep, voffA);
;             PG8_WAIT_V(8); PG8_WAIT_L(0); PG8_BAR; PG8_MMA(0, 0, At, B0); PG8_MMA(0, 1, At, B1); PG8_BAR; PG8_SCHED;
;             PG8_LDA(At, 0, 1); PG8_STAGE(PG8_SB(0, 0), b2, voffB); PG8_STAGE(PG8_SB(0, 1), b2 + hstepB, voffB); PG8_STAGE(PG8_SA(0, 0), a2, voffA);
;             PG8_WAIT_V(8); PG8_WAIT_L(0); PG8_BAR; PG8_MMA(1, 0, At, B0); PG8_MMA(1, 1, At, B1); PG8_BAR; PG8_SCHED;
.LBB0_1171:
	ds_read_b128 v[156:159], v152
	ds_read_b128 v[160:163], v152 offset:1024
	ds_read_b128 v[164:167], v152 offset:2048
	ds_read_b128 v[168:171], v152 offset:3072
	ds_read_b128 v[172:175], v153
	ds_read_b128 v[176:179], v153 offset:1024
	ds_read_b128 v[180:183], v153 offset:2048
	ds_read_b128 v[184:187], v153 offset:3072
	s_add_i32 s61, s34, 2
	s_add_u32 s0, s30, 0x80
	s_addc_u32 s1, s31, 0
	s_cmp_eq_u32 s49, s34
	s_cselect_b32 s34, s6, s0
	s_cselect_b32 s35, s7, s1
	s_cselect_b32 s1, s29, s59
	s_cselect_b32 s0, s28, s58
	s_cmp_eq_u32 s99, 0
	s_cbranch_scc1 .Lkr3_a
	s_add_i32 m0, s45, 0xffffff80
	s_nop 0
	global_load_lds_dwordx4 v[228:229], off offset:128
	s_add_i32 m0, s46, 0xffffff80
	s_nop 0
	global_load_lds_dwordx4 v[230:231], off offset:128
.Lkr3_a:
	v_lshl_add_u64 v[148:149], s[30:31], 0, v[140:141]
	s_add_i32 m0, s40, 0xc000
	ds_read_b128 v[188:191], v154
	ds_read_b128 v[192:195], v154 offset:1024
	ds_read_b128 v[196:199], v154 offset:2048
	ds_read_b128 v[200:203], v154 offset:3072
	ds_read_b128 v[204:207], v154 offset:4096
	ds_read_b128 v[212:215], v154 offset:5120
	ds_read_b128 v[216:219], v154 offset:6144
	ds_read_b128 v[220:223], v154 offset:7168
	global_load_lds_dwordx4 v[148:149], off
	v_lshl_add_u64 v[148:149], s[30:31], 0, v[142:143]
	s_add_i32 m0, s40, 0xe000
	s_nop 0
	global_load_lds_dwordx4 v[148:149], off
	s_waitcnt vmcnt(8)
	s_waitcnt lgkmcnt(0)
	s_barrier
	s_setprio 1
	s_waitcnt lgkmcnt(0)
	v_mfma_f32_16x16x32_bf16 v[126:129], v[156:159], v[188:191], v[126:129]
	v_mfma_f32_16x16x32_bf16 v[122:125], v[164:167], v[188:191], v[122:125]
	v_mfma_f32_16x16x32_bf16 v[110:113], v[156:159], v[196:199], v[110:113]
	v_mfma_f32_16x16x32_bf16 v[106:109], v[164:167], v[196:199], v[106:109]
	v_mfma_f32_16x16x32_bf16 v[94:97], v[156:159], v[204:207], v[94:97]
	v_mfma_f32_16x16x32_bf16 v[90:93], v[164:167], v[204:207], v[90:93]
	v_mfma_f32_16x16x32_bf16 v[78:81], v[156:159], v[216:219], v[78:81]
	v_mfma_f32_16x16x32_bf16 v[74:77], v[164:167], v[216:219], v[74:77]
	v_mfma_f32_16x16x32_bf16 v[126:129], v[160:163], v[192:195], v[126:129]
	v_mfma_f32_16x16x32_bf16 v[122:125], v[168:171], v[192:195], v[122:125]
	v_mfma_f32_16x16x32_bf16 v[110:113], v[160:163], v[200:203], v[110:113]
	v_mfma_f32_16x16x32_bf16 v[106:109], v[168:171], v[200:203], v[106:109]
	v_mfma_f32_16x16x32_bf16 v[94:97], v[160:163], v[212:215], v[94:97]
	v_mfma_f32_16x16x32_bf16 v[90:93], v[168:171], v[212:215], v[90:93]
	v_mfma_f32_16x16x32_bf16 v[78:81], v[160:163], v[220:223], v[78:81]
	v_mfma_f32_16x16x32_bf16 v[74:77], v[168:171], v[220:223], v[74:77]
	s_setprio 0
	s_setprio 1
	v_mfma_f32_16x16x32_bf16 v[118:121], v[172:175], v[188:191], v[118:121]
	v_mfma_f32_16x16x32_bf16 v[114:117], v[180:183], v[188:191], v[114:117]
	v_mfma_f32_16x16x32_bf16 v[102:105], v[172:175], v[196:199], v[102:105]
	v_mfma_f32_16x16x32_bf16 v[98:101], v[180:183], v[196:199], v[98:101]
	v_mfma_f32_16x16x32_bf16 v[86:89], v[172:175], v[204:207], v[86:89]
	v_mfma_f32_16x16x32_bf16 v[82:85], v[180:183], v[204:207], v[82:85]
	v_mfma_f32_16x16x32_bf16 v[70:73], v[172:175], v[216:219], v[70:73]
	v_mfma_f32_16x16x32_bf16 v[66:69], v[180:183], v[216:219], v[66:69]
	v_mfma_f32_16x16x32_bf16 v[118:121], v[176:179], v[192:195], v[118:121]
	v_mfma_f32_16x16x32_bf16 v[114:117], v[184:187], v[192:195], v[114:117]
	v_mfma_f32_16x16x32_bf16 v[102:105], v[176:179], v[200:203], v[102:105]
	v_mfma_f32_16x16x32_bf16 v[98:101], v[184:187], v[200:203], v[98:101]
	v_mfma_f32_16x16x32_bf16 v[86:89], v[176:179], v[212:215], v[86:89]
	v_mfma_f32_16x16x32_bf16 v[82:85], v[184:187], v[212:215], v[82:85]
	v_mfma_f32_16x16x32_bf16 v[70:73], v[176:179], v[220:223], v[70:73]
	v_mfma_f32_16x16x32_bf16 v[66:69], v[184:187], v[220:223], v[66:69]
	s_setprio 0
	s_barrier
	s_add_i32 s33, s52, s39
	v_lshl_add_u64 v[148:149], s[0:1], 0, v[132:133]
	s_mov_b32 m0, s33
	ds_read_b128 v[188:191], v154 offset:16384
	ds_read_b128 v[192:195], v154 offset:17408
	ds_read_b128 v[196:199], v154 offset:18432
	ds_read_b128 v[200:203], v154 offset:19456
	ds_read_b128 v[204:207], v154 offset:20480
	ds_read_b128 v[212:215], v154 offset:21504
	ds_read_b128 v[216:219], v154 offset:22528
	ds_read_b128 v[220:223], v154 offset:23552
	global_load_lds_dwordx4 v[148:149], off
	s_add_i32 m0, s33, 0x2000
	v_lshl_add_u64 v[208:209], s[0:1], 0, v[136:137]
	s_add_u32 s0, s0, s14
	s_addc_u32 s1, s1, s15
	s_add_i32 s33, s53, s39
	global_load_lds_dwordx4 v[208:209], off
	v_lshl_add_u64 v[224:225], s[0:1], 0, v[132:133]
	s_mov_b32 m0, s33
	v_lshl_add_u64 v[226:227], s[0:1], 0, v[136:137]
	global_load_lds_dwordx4 v[224:225], off
	s_add_i32 m0, s33, 0x2000
	v_lshl_add_u64 v[228:229], s[34:35], 0, v[130:131]
	global_load_lds_dwordx4 v[226:227], off
	v_lshl_add_u64 v[230:231], s[34:35], 0, v[134:135]
	s_waitcnt vmcnt(6)
	s_waitcnt lgkmcnt(0)
	s_barrier
; #define PG8_STAGE(bufoff, gbase, voff) do { _Pragma("unroll") for (int _i = 0; _i < 2; ++_i) \
;         __builtin_amdgcn_global_load_lds((const unsigned*)((const char*)(gbase) + (voff)[_i]), (PG8_LAS unsigned*)(lds + (bufoff) + ldsw + _i * 8192), 16, 0, 0); } while (0)
; #define PG8_LDA(dst, b, h) do { _Pragma("unroll") for (int m = 0; m < 4; ++m) { const bf16x8 f0_ = *(const PG8_LAS bf16x8*)(lds + PG8_SA(b, h) + aoff + m * 2048), f1_ = *(const PG8_LAS bf16x8*)(lds + PG8_SA(b, h) + aoff + m * 2048 + 1024); dst[m].set(f0_, f1_); } } while (0)
; #define PG8_LDB(dst, b, h) do { _Pragma("unroll") for (int n = 0; n < 2; ++n) { const bf16x8 f0_ = *(const PG8_LAS bf16x8*)(lds + PG8_SB(b, h) + boff + n * 2048), f1_ = *(const PG8_LAS bf16x8*)(lds + PG8_SB(b, h) + boff + n * 2048 + 1024); dst[n].set(f0_, f1_); } } while (0)
; #define PG8_WAIT_V(n) asm volatile("s_waitcnt vmcnt(" #n ")" ::: "memory")
; #define PG8_WAIT_L(n) asm volatile("s_waitcnt lgkmcnt(" #n ")" ::: "memory")
; #define PG8_BAR __builtin_amdgcn_s_barrier()
; #define PG8_SCHED __builtin_amdgcn_sched_barrier(0)
; template <class Epi, class Sched, bool ALIGN_EPI = false, bool SP2 = false>
; __device__ __forceinline__ void gemm_phase(PG8_LAS unsigned char* lds, const Gemm g, const Sched& S, const Epi& E) {
;     ...
;             PG8_WAIT_V(8); PG8_WAIT_L(0); PG8_BAR; PG8_MMA(1, 0, At, B0); PG8_MMA(1, 1, At, B1); PG8_BAR; PG8_SCHED;
;             PG8_LDB(B0, 1, 0); PG8_LDB(B1, 1, 1); PG8_SCHED; PG8_LDA(At, 1, 0); PG8_STAGE(PG8_SA(0, 1), a2 + hstep, voffA);
;             PG8_WAIT_V(8); PG8_WAIT_L(0); PG8_BAR; PG8_MMA(0, 0, At, B0); PG8_MMA(0, 1, At, B1); PG8_BAR; PG8_SCHED;
;             PG8_LDA(At, 1, 1); PG8_STAGE(PG8_SB(1, 0), b3, voffB); PG8_STAGE(PG8_SB(1, 1), b3 + hstepB, voffB); PG8_STAGE(PG8_SA(1, 0), a3, voffA);
	s_setprio 1
	s_waitcnt lgkmcnt(0)
	v_mfma_f32_16x16x32_bf16 v[62:65], v[156:159], v[188:191], v[62:65]
	v_mfma_f32_16x16x32_bf16 v[58:61], v[164:167], v[188:191], v[58:61]
	v_mfma_f32_16x16x32_bf16 v[46:49], v[156:159], v[196:199], v[46:49]
	v_mfma_f32_16x16x32_bf16 v[42:45], v[164:167], v[196:199], v[42:45]
	v_mfma_f32_16x16x32_bf16 v[30:33], v[156:159], v[204:207], v[30:33]
	v_mfma_f32_16x16x32_bf16 v[26:29], v[164:167], v[204:207], v[26:29]
	v_mfma_f32_16x16x32_bf16 v[14:17], v[156:159], v[216:219], v[14:17]
	v_mfma_f32_16x16x32_bf16 v[6:9], v[164:167], v[216:219], v[6:9]
	v_mfma_f32_16x16x32_bf16 v[62:65], v[160:163], v[192:195], v[62:65]
	v_mfma_f32_16x16x32_bf16 v[58:61], v[168:171], v[192:195], v[58:61]
	v_mfma_f32_16x16x32_bf16 v[46:49], v[160:163], v[200:203], v[46:49]
	v_mfma_f32_16x16x32_bf16 v[42:45], v[168:171], v[200:203], v[42:45]
	v_mfma_f32_16x16x32_bf16 v[30:33], v[160:163], v[212:215], v[30:33]
	v_mfma_f32_16x16x32_bf16 v[26:29], v[168:171], v[212:215], v[26:29]
	v_mfma_f32_16x16x32_bf16 v[14:17], v[160:163], v[220:223], v[14:17]
	v_mfma_f32_16x16x32_bf16 v[6:9], v[168:171], v[220:223], v[6:9]
	s_setprio 0
	s_setprio 1
	v_mfma_f32_16x16x32_bf16 v[54:57], v[172:175], v[188:191], v[54:57]
	v_mfma_f32_16x16x32_bf16 v[50:53], v[180:183], v[188:191], v[50:53]
	v_mfma_f32_16x16x32_bf16 v[38:41], v[172:175], v[196:199], v[38:41]
	v_mfma_f32_16x16x32_bf16 v[34:37], v[180:183], v[196:199], v[34:37]
	v_mfma_f32_16x16x32_bf16 v[22:25], v[172:175], v[204:207], v[22:25]
	v_mfma_f32_16x16x32_bf16 v[18:21], v[180:183], v[204:207], v[18:21]
	v_mfma_f32_16x16x32_bf16 v[10:13], v[172:175], v[216:219], v[10:13]
	v_mfma_f32_16x16x32_bf16 v[2:5], v[180:183], v[216:219], v[2:5]
	v_mfma_f32_16x16x32_bf16 v[54:57], v[176:179], v[192:195], v[54:57]
	v_mfma_f32_16x16x32_bf16 v[50:53], v[184:187], v[192:195], v[50:53]
	v_mfma_f32_16x16x32_bf16 v[38:41], v[176:179], v[200:203], v[38:41]
	v_mfma_f32_16x16x32_bf16 v[34:37], v[184:187], v[200:203], v[34:37]
	v_mfma_f32_16x16x32_bf16 v[22:25], v[176:179], v[212:215], v[22:25]
	v_mfma_f32_16x16x32_bf16 v[18:21], v[184:187], v[212:215], v[18:21]
	v_mfma_f32_16x16x32_bf16 v[10:13], v[176:179], v[220:223], v[10:13]
	v_mfma_f32_16x16x32_bf16 v[2:5], v[184:187], v[220:223], v[2:5]
	s_setprio 0
	s_barrier
	s_add_i32 s33, 0, 0x18000
	s_add_i32 s63, 0, 0x1c000
	v_add_u32_e32 v168, s33, v1
	v_add_u32_e32 v184, s63, v1
	ds_read_b128 v[156:159], v168
	ds_read_b128 v[160:163], v168 offset:1024
	ds_read_b128 v[164:167], v168 offset:2048
	ds_read_b128 v[168:171], v168 offset:3072
	ds_read_b128 v[172:175], v184
	ds_read_b128 v[176:179], v184 offset:1024
	ds_read_b128 v[180:183], v184 offset:2048
	ds_read_b128 v[184:187], v184 offset:3072
	s_add_u32 s0, s34, s12
	s_addc_u32 s1, s35, s13
	s_mov_b32 m0, s42
	v_lshl_add_u64 v[232:233], s[0:1], 0, v[130:131]
	ds_read_b128 v[188:191], v154 offset:32768
	ds_read_b128 v[192:195], v154 offset:33792
	ds_read_b128 v[196:199], v154 offset:34816
	ds_read_b128 v[200:203], v154 offset:35840
	ds_read_b128 v[204:207], v154 offset:36864
	ds_read_b128 v[212:215], v154 offset:37888
	ds_read_b128 v[216:219], v154 offset:38912
	ds_read_b128 v[220:223], v154 offset:39936
	s_mov_b32 m0, s40
	s_nop 0
	global_load_lds_dwordx4 v[228:229], off
	s_mov_b32 m0, s41
	s_nop 0
	global_load_lds_dwordx4 v[230:231], off
	s_mov_b32 m0, s42
	s_nop 0
	global_load_lds_dwordx4 v[232:233], off
	v_lshl_add_u64 v[232:233], s[0:1], 0, v[134:135]
	s_mov_b32 m0, s43
	s_nop 0
	global_load_lds_dwordx4 v[232:233], off
	s_waitcnt vmcnt(8)
	s_waitcnt lgkmcnt(0)
	s_barrier
	s_setprio 1
	s_waitcnt lgkmcnt(0)
	v_mfma_f32_16x16x32_bf16 v[126:129], v[156:159], v[188:191], v[126:129]
	v_mfma_f32_16x16x32_bf16 v[122:125], v[164:167], v[188:191], v[122:125]
	v_mfma_f32_16x16x32_bf16 v[110:113], v[156:159], v[196:199], v[110:113]
	v_mfma_f32_16x16x32_bf16 v[106:109], v[164:167], v[196:199], v[106:109]
	v_mfma_f32_16x16x32_bf16 v[94:97], v[156:159], v[204:207], v[94:97]
	v_mfma_f32_16x16x32_bf16 v[90:93], v[164:167], v[204:207], v[90:93]
	v_mfma_f32_16x16x32_bf16 v[78:81], v[156:159], v[216:219], v[78:81]
	v_mfma_f32_16x16x32_bf16 v[74:77], v[164:167], v[216:219], v[74:77]
	v_mfma_f32_16x16x32_bf16 v[126:129], v[160:163], v[192:195], v[126:129]
	v_mfma_f32_16x16x32_bf16 v[122:125], v[168:171], v[192:195], v[122:125]
	v_mfma_f32_16x16x32_bf16 v[110:113], v[160:163], v[200:203], v[110:113]
	v_mfma_f32_16x16x32_bf16 v[106:109], v[168:171], v[200:203], v[106:109]
	v_mfma_f32_16x16x32_bf16 v[94:97], v[160:163], v[212:215], v[94:97]
	v_mfma_f32_16x16x32_bf16 v[90:93], v[168:171], v[212:215], v[90:93]
	v_mfma_f32_16x16x32_bf16 v[78:81], v[160:163], v[220:223], v[78:81]
	v_mfma_f32_16x16x32_bf16 v[74:77], v[168:171], v[220:223], v[74:77]
	s_setprio 0
	s_setprio 1
	v_mfma_f32_16x16x32_bf16 v[118:121], v[172:175], v[188:191], v[118:121]
	v_mfma_f32_16x16x32_bf16 v[114:117], v[180:183], v[188:191], v[114:117]
	v_mfma_f32_16x16x32_bf16 v[102:105], v[172:175], v[196:199], v[102:105]
	v_mfma_f32_16x16x32_bf16 v[98:101], v[180:183], v[196:199], v[98:101]
	v_mfma_f32_16x16x32_bf16 v[86:89], v[172:175], v[204:207], v[86:89]
	v_mfma_f32_16x16x32_bf16 v[82:85], v[180:183], v[204:207], v[82:85]
	v_mfma_f32_16x16x32_bf16 v[70:73], v[172:175], v[216:219], v[70:73]
	v_mfma_f32_16x16x32_bf16 v[66:69], v[180:183], v[216:219], v[66:69]
	v_mfma_f32_16x16x32_bf16 v[118:121], v[176:179], v[192:195], v[118:121]
	v_mfma_f32_16x16x32_bf16 v[114:117], v[184:187], v[192:195], v[114:117]
	v_mfma_f32_16x16x32_bf16 v[102:105], v[176:179], v[200:203], v[102:105]
	v_mfma_f32_16x16x32_bf16 v[98:101], v[184:187], v[200:203], v[98:101]
	v_mfma_f32_16x16x32_bf16 v[86:89], v[176:179], v[212:215], v[86:89]
	v_mfma_f32_16x16x32_bf16 v[82:85], v[184:187], v[212:215], v[82:85]
	v_mfma_f32_16x16x32_bf16 v[70:73], v[176:179], v[220:223], v[70:73]
	v_mfma_f32_16x16x32_bf16 v[66:69], v[184:187], v[220:223], v[66:69]
	s_setprio 0
	s_barrier
	s_add_i32 s0, s33, s39
	s_add_i32 m0, s0, 0xffffff80
	ds_read_b128 v[188:191], v154 offset:49152
	ds_read_b128 v[192:195], v154 offset:50176
	ds_read_b128 v[196:199], v154 offset:51200
	ds_read_b128 v[200:203], v154 offset:52224
	ds_read_b128 v[204:207], v154 offset:53248
	ds_read_b128 v[212:215], v154 offset:54272
	ds_read_b128 v[216:219], v154 offset:55296
	ds_read_b128 v[220:223], v154 offset:56320
	global_load_lds_dwordx4 v[148:149], off offset:128
	s_add_i32 m0, s0, 0x1f80
	s_add_i32 s0, s63, s39
	global_load_lds_dwordx4 v[208:209], off offset:128
	s_add_i32 m0, s0, 0xffffff80
	s_nop 0
	global_load_lds_dwordx4 v[224:225], off offset:128
	s_add_i32 m0, s0, 0x1f80
	s_nop 0
	global_load_lds_dwordx4 v[226:227], off offset:128
	s_cmp_ge_i32 s61, s47
	s_cbranch_scc0 .Lkr3_b
	s_add_i32 m0, s45, 0xffffff80
	s_nop 0
	global_load_lds_dwordx4 v[228:229], off offset:128
	s_add_i32 m0, s46, 0xffffff80
	s_nop 0
	global_load_lds_dwordx4 v[230:231], off offset:128

; #define PG8_STAGE(bufoff, gbase, voff) do { _Pragma("unroll") for (int _i = 0; _i < 2; ++_i) \
;         __builtin_amdgcn_global_load_lds((const unsigned*)((const char*)(gbase) + (voff)[_i]), (PG8_LAS unsigned*)(lds + (bufoff) + ldsw + _i * 8192), 16, 0, 0); } while (0)
; #define PG8_LDA(dst, b, h) do { _Pragma("unroll") for (int m = 0; m < 4; ++m) { const bf16x8 f0_ = *(const PG8_LAS bf16x8*)(lds + PG8_SA(b, h) + aoff + m * 2048), f1_ = *(const PG8_LAS bf16x8*)(lds + PG8_SA(b, h) + aoff + m * 2048 + 1024); dst[m].set(f0_, f1_); } } while (0)
; #define PG8_LDB(dst, b, h) do { _Pragma("unroll") for (int n = 0; n < 2; ++n) { const bf16x8 f0_ = *(const PG8_LAS bf16x8*)(lds + PG8_SB(b, h) + boff + n * 2048), f1_ = *(const PG8_LAS bf16x8*)(lds + PG8_SB(b, h) + boff + n * 2048 + 1024); dst[n].set(f0_, f1_); } } while (0)
; #define PG8_WAIT_V(n) asm volatile("s_waitcnt vmcnt(" #n ")" ::: "memory")
; #define PG8_WAIT_L(n) asm volatile("s_waitcnt lgkmcnt(" #n ")" ::: "memory")
; #define PG8_BAR __builtin_amdgcn_s_barrier()
; #define PG8_SCHED __builtin_amdgcn_sched_barrier(0)
; template <class Epi, class Sched, bool ALIGN_EPI = false, bool SP2 = false>
; __device__ __forceinline__ void gemm_phase(PG8_LAS unsigned char* lds, const Gemm g, const Sched& S, const Epi& E) {
;     ...
;             const bool last = (t == nt - 2);
;             const char* a1 = cA + (size_t)(t + 1) * kstep;
;             const char* a2 = last ? nA : cA + (size_t)(t + 2) * kstep; const char* b2 = last ? nB : cB + (size_t)(t + 2) * kstep;
;             const char* a3 = a2 + kstep; const char* b3 = b2 + kstep;
;             if (last && has_next) S.a_ready(nxt);
;             if constexpr (SP2) {
;             PG8_LDB(B0, 0, 0); PG8_LDB(B1, 0, 1); PG8_SCHED; PG8_LDA(At, 0, 0); PG8_STAGE(PG8_SA(1, 1), a1 + hstep, voffA);
;             PG8_WAIT_V(8); PG8_WAIT_L(0); PG8_BAR; PG8_MMA(0, 0, At, B0); PG8_MMA(0, 1, At, B1); PG8_BAR; PG8_SCHED;
;             PG8_LDA(At, 0, 1); PG8_STAGE(PG8_SB(0, 0), b2, voffB); PG8_STAGE(PG8_SB(0, 1), b2 + hstepB, voffB); PG8_STAGE(PG8_SA(0, 0), a2, voffA);
;             PG8_WAIT_V(8); PG8_WAIT_L(0); PG8_BAR; PG8_MMA(1, 0, At, B0); PG8_MMA(1, 1, At, B1); PG8_BAR; PG8_SCHED;
.LBB0_1592:
	ds_read_b128 v[156:159], v152
	ds_read_b128 v[160:163], v152 offset:1024
	ds_read_b128 v[164:167], v152 offset:2048
	ds_read_b128 v[168:171], v152 offset:3072
	ds_read_b128 v[172:175], v153
	ds_read_b128 v[176:179], v153 offset:1024
	ds_read_b128 v[180:183], v153 offset:2048
	ds_read_b128 v[184:187], v153 offset:3072
	s_add_i32 s61, s34, 2
	s_add_u32 s0, s30, 0x80
	s_addc_u32 s1, s31, 0
	s_cmp_eq_u32 s49, s34
	s_cselect_b32 s34, s6, s0
	s_cselect_b32 s35, s7, s1
	s_cselect_b32 s1, s29, s59
	s_cselect_b32 s0, s28, s58
	s_cmp_eq_u32 s99, 0
	s_cbranch_scc1 .Lkr4_a
	s_add_i32 m0, s46, 0xffffff80
	s_nop 0
	global_load_lds_dwordx4 v[228:229], off offset:128
	s_add_i32 m0, s47, 0xffffff80
	s_nop 0
	global_load_lds_dwordx4 v[230:231], off offset:128
.Lkr4_a:
	v_lshl_add_u64 v[148:149], s[30:31], 0, v[140:141]
	s_add_i32 m0, s40, 0xc000
	ds_read_b128 v[188:191], v154
	ds_read_b128 v[192:195], v154 offset:1024
	ds_read_b128 v[196:199], v154 offset:2048
	ds_read_b128 v[200:203], v154 offset:3072
	ds_read_b128 v[204:207], v154 offset:4096
	ds_read_b128 v[212:215], v154 offset:5120
	ds_read_b128 v[216:219], v154 offset:6144
	ds_read_b128 v[220:223], v154 offset:7168
	global_load_lds_dwordx4 v[148:149], off
	v_lshl_add_u64 v[148:149], s[30:31], 0, v[142:143]
	s_add_i32 m0, s40, 0xe000
	s_nop 0
	global_load_lds_dwordx4 v[148:149], off
	s_waitcnt vmcnt(8)
	s_waitcnt lgkmcnt(0)
	s_barrier
	s_setprio 1
	s_waitcnt lgkmcnt(0)
	v_mfma_f32_16x16x32_bf16 v[126:129], v[156:159], v[188:191], v[126:129]
	v_mfma_f32_16x16x32_bf16 v[122:125], v[164:167], v[188:191], v[122:125]
	v_mfma_f32_16x16x32_bf16 v[110:113], v[156:159], v[196:199], v[110:113]
	v_mfma_f32_16x16x32_bf16 v[106:109], v[164:167], v[196:199], v[106:109]
	v_mfma_f32_16x16x32_bf16 v[94:97], v[156:159], v[204:207], v[94:97]
	v_mfma_f32_16x16x32_bf16 v[90:93], v[164:167], v[204:207], v[90:93]
	v_mfma_f32_16x16x32_bf16 v[78:81], v[156:159], v[216:219], v[78:81]
	v_mfma_f32_16x16x32_bf16 v[74:77], v[164:167], v[216:219], v[74:77]
	v_mfma_f32_16x16x32_bf16 v[126:129], v[160:163], v[192:195], v[126:129]
	v_mfma_f32_16x16x32_bf16 v[122:125], v[168:171], v[192:195], v[122:125]
	v_mfma_f32_16x16x32_bf16 v[110:113], v[160:163], v[200:203], v[110:113]
	v_mfma_f32_16x16x32_bf16 v[106:109], v[168:171], v[200:203], v[106:109]
	v_mfma_f32_16x16x32_bf16 v[94:97], v[160:163], v[212:215], v[94:97]
	v_mfma_f32_16x16x32_bf16 v[90:93], v[168:171], v[212:215], v[90:93]
	v_mfma_f32_16x16x32_bf16 v[78:81], v[160:163], v[220:223], v[78:81]
	v_mfma_f32_16x16x32_bf16 v[74:77], v[168:171], v[220:223], v[74:77]
	s_setprio 0
	s_setprio 1
	v_mfma_f32_16x16x32_bf16 v[118:121], v[172:175], v[188:191], v[118:121]
	v_mfma_f32_16x16x32_bf16 v[114:117], v[180:183], v[188:191], v[114:117]
	v_mfma_f32_16x16x32_bf16 v[102:105], v[172:175], v[196:199], v[102:105]
	v_mfma_f32_16x16x32_bf16 v[98:101], v[180:183], v[196:199], v[98:101]
	v_mfma_f32_16x16x32_bf16 v[86:89], v[172:175], v[204:207], v[86:89]
	v_mfma_f32_16x16x32_bf16 v[82:85], v[180:183], v[204:207], v[82:85]
	v_mfma_f32_16x16x32_bf16 v[70:73], v[172:175], v[216:219], v[70:73]
	v_mfma_f32_16x16x32_bf16 v[66:69], v[180:183], v[216:219], v[66:69]
	v_mfma_f32_16x16x32_bf16 v[118:121], v[176:179], v[192:195], v[118:121]
	v_mfma_f32_16x16x32_bf16 v[114:117], v[184:187], v[192:195], v[114:117]
	v_mfma_f32_16x16x32_bf16 v[102:105], v[176:179], v[200:203], v[102:105]
	v_mfma_f32_16x16x32_bf16 v[98:101], v[184:187], v[200:203], v[98:101]
	v_mfma_f32_16x16x32_bf16 v[86:89], v[176:179], v[212:215], v[86:89]
	v_mfma_f32_16x16x32_bf16 v[82:85], v[184:187], v[212:215], v[82:85]
	v_mfma_f32_16x16x32_bf16 v[70:73], v[176:179], v[220:223], v[70:73]
	v_mfma_f32_16x16x32_bf16 v[66:69], v[184:187], v[220:223], v[66:69]
	s_setprio 0
	s_barrier
	s_add_i32 s33, s52, s39
	v_lshl_add_u64 v[148:149], s[0:1], 0, v[132:133]
	s_mov_b32 m0, s33
	ds_read_b128 v[188:191], v154 offset:16384
	ds_read_b128 v[192:195], v154 offset:17408
	ds_read_b128 v[196:199], v154 offset:18432
	ds_read_b128 v[200:203], v154 offset:19456
	ds_read_b128 v[204:207], v154 offset:20480
	ds_read_b128 v[212:215], v154 offset:21504
	ds_read_b128 v[216:219], v154 offset:22528
	ds_read_b128 v[220:223], v154 offset:23552
	global_load_lds_dwordx4 v[148:149], off
	s_add_i32 m0, s33, 0x2000
	v_lshl_add_u64 v[208:209], s[0:1], 0, v[136:137]
	s_add_u32 s0, s0, s14
	s_addc_u32 s1, s1, s15
	s_add_i32 s33, s53, s39
	global_load_lds_dwordx4 v[208:209], off
	v_lshl_add_u64 v[224:225], s[0:1], 0, v[132:133]
	s_mov_b32 m0, s33
	v_lshl_add_u64 v[226:227], s[0:1], 0, v[136:137]
	global_load_lds_dwordx4 v[224:225], off
	s_add_i32 m0, s33, 0x2000
	v_lshl_add_u64 v[228:229], s[34:35], 0, v[130:131]
	global_load_lds_dwordx4 v[226:227], off
	v_lshl_add_u64 v[230:231], s[34:35], 0, v[134:135]
	s_waitcnt vmcnt(6)
	s_waitcnt lgkmcnt(0)
	s_barrier
; #define PG8_STAGE(bufoff, gbase, voff) do { _Pragma("unroll") for (int _i = 0; _i < 2; ++_i) \
;         __builtin_amdgcn_global_load_lds((const unsigned*)((const char*)(gbase) + (voff)[_i]), (PG8_LAS unsigned*)(lds + (bufoff) + ldsw + _i * 8192), 16, 0, 0); } while (0)
; #define PG8_LDA(dst, b, h) do { _Pragma("unroll") for (int m = 0; m < 4; ++m) { const bf16x8 f0_ = *(const PG8_LAS bf16x8*)(lds + PG8_SA(b, h) + aoff + m * 2048), f1_ = *(const PG8_LAS bf16x8*)(lds + PG8_SA(b, h) + aoff + m * 2048 + 1024); dst[m].set(f0_, f1_); } } while (0)
; #define PG8_LDB(dst, b, h) do { _Pragma("unroll") for (int n = 0; n < 2; ++n) { const bf16x8 f0_ = *(const PG8_LAS bf16x8*)(lds + PG8_SB(b, h) + boff + n * 2048), f1_ = *(const PG8_LAS bf16x8*)(lds + PG8_SB(b, h) + boff + n * 2048 + 1024); dst[n].set(f0_, f1_); } } while (0)
; #define PG8_WAIT_V(n) asm volatile("s_waitcnt vmcnt(" #n ")" ::: "memory")
; #define PG8_WAIT_L(n) asm volatile("s_waitcnt lgkmcnt(" #n ")" ::: "memory")
; #define PG8_BAR __builtin_amdgcn_s_barrier()
; #define PG8_SCHED __builtin_amdgcn_sched_barrier(0)
; template <class Epi, class Sched, bool ALIGN_EPI = false, bool SP2 = false>
; __device__ __forceinline__ void gemm_phase(PG8_LAS unsigned char* lds, const Gemm g, const Sched& S, const Epi& E) {
;     ...
;             PG8_WAIT_V(8); PG8_WAIT_L(0); PG8_BAR; PG8_MMA(1, 0, At, B0); PG8_MMA(1, 1, At, B1); PG8_BAR; PG8_SCHED;
;             PG8_LDB(B0, 1, 0); PG8_LDB(B1, 1, 1); PG8_SCHED; PG8_LDA(At, 1, 0); PG8_STAGE(PG8_SA(0, 1), a2 + hstep, voffA);
;             PG8_WAIT_V(8); PG8_WAIT_L(0); PG8_BAR; PG8_MMA(0, 0, At, B0); PG8_MMA(0, 1, At, B1); PG8_BAR; PG8_SCHED;
;             PG8_LDA(At, 1, 1); PG8_STAGE(PG8_SB(1, 0), b3, voffB); PG8_STAGE(PG8_SB(1, 1), b3 + hstepB, voffB); PG8_STAGE(PG8_SA(1, 0), a3, voffA);
	s_setprio 1
	s_waitcnt lgkmcnt(0)
	v_mfma_f32_16x16x32_bf16 v[62:65], v[156:159], v[188:191], v[62:65]
	v_mfma_f32_16x16x32_bf16 v[58:61], v[164:167], v[188:191], v[58:61]
	v_mfma_f32_16x16x32_bf16 v[46:49], v[156:159], v[196:199], v[46:49]
	v_mfma_f32_16x16x32_bf16 v[42:45], v[164:167], v[196:199], v[42:45]
	v_mfma_f32_16x16x32_bf16 v[30:33], v[156:159], v[204:207], v[30:33]
	v_mfma_f32_16x16x32_bf16 v[26:29], v[164:167], v[204:207], v[26:29]
	v_mfma_f32_16x16x32_bf16 v[14:17], v[156:159], v[216:219], v[14:17]
	v_mfma_f32_16x16x32_bf16 v[6:9], v[164:167], v[216:219], v[6:9]
	v_mfma_f32_16x16x32_bf16 v[62:65], v[160:163], v[192:195], v[62:65]
	v_mfma_f32_16x16x32_bf16 v[58:61], v[168:171], v[192:195], v[58:61]
	v_mfma_f32_16x16x32_bf16 v[46:49], v[160:163], v[200:203], v[46:49]
	v_mfma_f32_16x16x32_bf16 v[42:45], v[168:171], v[200:203], v[42:45]
	v_mfma_f32_16x16x32_bf16 v[30:33], v[160:163], v[212:215], v[30:33]
	v_mfma_f32_16x16x32_bf16 v[26:29], v[168:171], v[212:215], v[26:29]
	v_mfma_f32_16x16x32_bf16 v[14:17], v[160:163], v[220:223], v[14:17]
	v_mfma_f32_16x16x32_bf16 v[6:9], v[168:171], v[220:223], v[6:9]
	s_setprio 0
	s_setprio 1
	v_mfma_f32_16x16x32_bf16 v[54:57], v[172:175], v[188:191], v[54:57]
	v_mfma_f32_16x16x32_bf16 v[50:53], v[180:183], v[188:191], v[50:53]
	v_mfma_f32_16x16x32_bf16 v[38:41], v[172:175], v[196:199], v[38:41]
	v_mfma_f32_16x16x32_bf16 v[34:37], v[180:183], v[196:199], v[34:37]
	v_mfma_f32_16x16x32_bf16 v[22:25], v[172:175], v[204:207], v[22:25]
	v_mfma_f32_16x16x32_bf16 v[18:21], v[180:183], v[204:207], v[18:21]
	v_mfma_f32_16x16x32_bf16 v[10:13], v[172:175], v[216:219], v[10:13]
	v_mfma_f32_16x16x32_bf16 v[2:5], v[180:183], v[216:219], v[2:5]
	v_mfma_f32_16x16x32_bf16 v[54:57], v[176:179], v[192:195], v[54:57]
	v_mfma_f32_16x16x32_bf16 v[50:53], v[184:187], v[192:195], v[50:53]
	v_mfma_f32_16x16x32_bf16 v[38:41], v[176:179], v[200:203], v[38:41]
	v_mfma_f32_16x16x32_bf16 v[34:37], v[184:187], v[200:203], v[34:37]
	v_mfma_f32_16x16x32_bf16 v[22:25], v[176:179], v[212:215], v[22:25]
	v_mfma_f32_16x16x32_bf16 v[18:21], v[184:187], v[212:215], v[18:21]
	v_mfma_f32_16x16x32_bf16 v[10:13], v[176:179], v[220:223], v[10:13]
	v_mfma_f32_16x16x32_bf16 v[2:5], v[184:187], v[220:223], v[2:5]
	s_setprio 0
	s_barrier
	s_add_i32 s33, 0, 0x18000
	s_add_i32 s63, 0, 0x1c000
	v_add_u32_e32 v168, s33, v1
	v_add_u32_e32 v184, s63, v1
	ds_read_b128 v[156:159], v168
	ds_read_b128 v[160:163], v168 offset:1024
	ds_read_b128 v[164:167], v168 offset:2048
	ds_read_b128 v[168:171], v168 offset:3072
	ds_read_b128 v[172:175], v184
	ds_read_b128 v[176:179], v184 offset:1024
	ds_read_b128 v[180:183], v184 offset:2048
	ds_read_b128 v[184:187], v184 offset:3072
	s_add_u32 s0, s34, s12
	s_addc_u32 s1, s35, s13
	s_mov_b32 m0, s42
	v_lshl_add_u64 v[232:233], s[0:1], 0, v[130:131]
	ds_read_b128 v[188:191], v154 offset:32768
	ds_read_b128 v[192:195], v154 offset:33792
	ds_read_b128 v[196:199], v154 offset:34816
	ds_read_b128 v[200:203], v154 offset:35840
	ds_read_b128 v[204:207], v154 offset:36864
	ds_read_b128 v[212:215], v154 offset:37888
	ds_read_b128 v[216:219], v154 offset:38912
	ds_read_b128 v[220:223], v154 offset:39936
	s_mov_b32 m0, s40
	s_nop 0
	global_load_lds_dwordx4 v[228:229], off
	s_mov_b32 m0, s41
	s_nop 0
	global_load_lds_dwordx4 v[230:231], off
	s_mov_b32 m0, s42
	s_nop 0
	global_load_lds_dwordx4 v[232:233], off
	v_lshl_add_u64 v[232:233], s[0:1], 0, v[134:135]
	s_mov_b32 m0, s43
	s_nop 0
	global_load_lds_dwordx4 v[232:233], off
	s_waitcnt vmcnt(8)
	s_waitcnt lgkmcnt(0)
	s_barrier
	s_setprio 1
	s_waitcnt lgkmcnt(0)
	v_mfma_f32_16x16x32_bf16 v[126:129], v[156:159], v[188:191], v[126:129]
	v_mfma_f32_16x16x32_bf16 v[122:125], v[164:167], v[188:191], v[122:125]
	v_mfma_f32_16x16x32_bf16 v[110:113], v[156:159], v[196:199], v[110:113]
	v_mfma_f32_16x16x32_bf16 v[106:109], v[164:167], v[196:199], v[106:109]
	v_mfma_f32_16x16x32_bf16 v[94:97], v[156:159], v[204:207], v[94:97]
	v_mfma_f32_16x16x32_bf16 v[90:93], v[164:167], v[204:207], v[90:93]
	v_mfma_f32_16x16x32_bf16 v[78:81], v[156:159], v[216:219], v[78:81]
	v_mfma_f32_16x16x32_bf16 v[74:77], v[164:167], v[216:219], v[74:77]
	v_mfma_f32_16x16x32_bf16 v[126:129], v[160:163], v[192:195], v[126:129]
	v_mfma_f32_16x16x32_bf16 v[122:125], v[168:171], v[192:195], v[122:125]
	v_mfma_f32_16x16x32_bf16 v[110:113], v[160:163], v[200:203], v[110:113]
	v_mfma_f32_16x16x32_bf16 v[106:109], v[168:171], v[200:203], v[106:109]
	v_mfma_f32_16x16x32_bf16 v[94:97], v[160:163], v[212:215], v[94:97]
	v_mfma_f32_16x16x32_bf16 v[90:93], v[168:171], v[212:215], v[90:93]
	v_mfma_f32_16x16x32_bf16 v[78:81], v[160:163], v[220:223], v[78:81]
	v_mfma_f32_16x16x32_bf16 v[74:77], v[168:171], v[220:223], v[74:77]
	s_setprio 0
	s_setprio 1
	v_mfma_f32_16x16x32_bf16 v[118:121], v[172:175], v[188:191], v[118:121]
	v_mfma_f32_16x16x32_bf16 v[114:117], v[180:183], v[188:191], v[114:117]
	v_mfma_f32_16x16x32_bf16 v[102:105], v[172:175], v[196:199], v[102:105]
	v_mfma_f32_16x16x32_bf16 v[98:101], v[180:183], v[196:199], v[98:101]
	v_mfma_f32_16x16x32_bf16 v[86:89], v[172:175], v[204:207], v[86:89]
	v_mfma_f32_16x16x32_bf16 v[82:85], v[180:183], v[204:207], v[82:85]
	v_mfma_f32_16x16x32_bf16 v[70:73], v[172:175], v[216:219], v[70:73]
	v_mfma_f32_16x16x32_bf16 v[66:69], v[180:183], v[216:219], v[66:69]
	v_mfma_f32_16x16x32_bf16 v[118:121], v[176:179], v[192:195], v[118:121]
	v_mfma_f32_16x16x32_bf16 v[114:117], v[184:187], v[192:195], v[114:117]
	v_mfma_f32_16x16x32_bf16 v[102:105], v[176:179], v[200:203], v[102:105]
	v_mfma_f32_16x16x32_bf16 v[98:101], v[184:187], v[200:203], v[98:101]
	v_mfma_f32_16x16x32_bf16 v[86:89], v[176:179], v[212:215], v[86:89]
	v_mfma_f32_16x16x32_bf16 v[82:85], v[184:187], v[212:215], v[82:85]
	v_mfma_f32_16x16x32_bf16 v[70:73], v[176:179], v[220:223], v[70:73]
	v_mfma_f32_16x16x32_bf16 v[66:69], v[184:187], v[220:223], v[66:69]
	s_setprio 0
	s_barrier
	s_add_i32 s0, s33, s39
	s_add_i32 m0, s0, 0xffffff80
	ds_read_b128 v[188:191], v154 offset:49152
	ds_read_b128 v[192:195], v154 offset:50176
	ds_read_b128 v[196:199], v154 offset:51200
	ds_read_b128 v[200:203], v154 offset:52224
	ds_read_b128 v[204:207], v154 offset:53248
	ds_read_b128 v[212:215], v154 offset:54272
	ds_read_b128 v[216:219], v154 offset:55296
	ds_read_b128 v[220:223], v154 offset:56320
	global_load_lds_dwordx4 v[148:149], off offset:128
	s_add_i32 m0, s0, 0x1f80
	s_add_i32 s0, s63, s39
	global_load_lds_dwordx4 v[208:209], off offset:128
	s_add_i32 m0, s0, 0xffffff80
	s_nop 0
	global_load_lds_dwordx4 v[224:225], off offset:128
	s_add_i32 m0, s0, 0x1f80
	s_nop 0
	global_load_lds_dwordx4 v[226:227], off offset:128
	s_cmp_ge_i32 s61, s48
	s_cbranch_scc0 .Lkr4_b
	s_add_i32 m0, s46, 0xffffff80
	s_nop 0
	global_load_lds_dwordx4 v[228:229], off offset:128
	s_add_i32 m0, s47, 0xffffff80
	s_nop 0
	global_load_lds_dwordx4 v[230:231], off offset:128

; #define PG8_STAGE(bufoff, gbase, voff) do { _Pragma("unroll") for (int _i = 0; _i < 2; ++_i) \
;         __builtin_amdgcn_global_load_lds((const unsigned*)((const char*)(gbase) + (voff)[_i]), (PG8_LAS unsigned*)(lds + (bufoff) + ldsw + _i * 8192), 16, 0, 0); } while (0)
; #define PG8_LDA(dst, b, h) do { _Pragma("unroll") for (int m = 0; m < 4; ++m) { const bf16x8 f0_ = *(const PG8_LAS bf16x8*)(lds + PG8_SA(b, h) + aoff + m * 2048), f1_ = *(const PG8_LAS bf16x8*)(lds + PG8_SA(b, h) + aoff + m * 2048 + 1024); dst[m].set(f0_, f1_); } } while (0)
; #define PG8_LDB(dst, b, h) do { _Pragma("unroll") for (int n = 0; n < 2; ++n) { const bf16x8 f0_ = *(const PG8_LAS bf16x8*)(lds + PG8_SB(b, h) + boff + n * 2048), f1_ = *(const PG8_LAS bf16x8*)(lds + PG8_SB(b, h) + boff + n * 2048 + 1024); dst[n].set(f0_, f1_); } } while (0)
; #define PG8_WAIT_V(n) asm volatile("s_waitcnt vmcnt(" #n ")" ::: "memory")
; #define PG8_WAIT_L(n) asm volatile("s_waitcnt lgkmcnt(" #n ")" ::: "memory")
; #define PG8_BAR __builtin_amdgcn_s_barrier()
; #define PG8_SCHED __builtin_amdgcn_sched_barrier(0)
; template <class Epi, class Sched, bool ALIGN_EPI = false, bool SP2 = false>
; __device__ __forceinline__ void gemm_phase(PG8_LAS unsigned char* lds, const Gemm g, const Sched& S, const Epi& E) {
;     ...
;             const bool last = (t == nt - 2);
;             const char* a1 = cA + (size_t)(t + 1) * kstep;
;             const char* a2 = last ? nA : cA + (size_t)(t + 2) * kstep; const char* b2 = last ? nB : cB + (size_t)(t + 2) * kstep;
;             const char* a3 = a2 + kstep; const char* b3 = b2 + kstep;
;             if (last && has_next) S.a_ready(nxt);
;             if constexpr (SP2) {
;             PG8_LDB(B0, 0, 0); PG8_LDB(B1, 0, 1); PG8_SCHED; PG8_LDA(At, 0, 0); PG8_STAGE(PG8_SA(1, 1), a1 + hstep, voffA);
;             PG8_WAIT_V(8); PG8_WAIT_L(0); PG8_BAR; PG8_MMA(0, 0, At, B0); PG8_MMA(0, 1, At, B1); PG8_BAR; PG8_SCHED;
;             PG8_LDA(At, 0, 1); PG8_STAGE(PG8_SB(0, 0), b2, voffB); PG8_STAGE(PG8_SB(0, 1), b2 + hstepB, voffB); PG8_STAGE(PG8_SA(0, 0), a2, voffA);
;             PG8_WAIT_V(8); PG8_WAIT_L(0); PG8_BAR; PG8_MMA(1, 0, At, B0); PG8_MMA(1, 1, At, B1); PG8_BAR; PG8_SCHED;
.LBB0_1625:
	ds_read_b128 v[18:21], v197
	ds_read_b128 v[22:25], v197 offset:1024
	ds_read_b128 v[26:29], v197 offset:2048
	ds_read_b128 v[30:33], v197 offset:3072
	ds_read_b128 v[2:5], v198
	ds_read_b128 v[6:9], v198 offset:1024
	ds_read_b128 v[10:13], v198 offset:2048
	ds_read_b128 v[14:17], v198 offset:3072
	s_add_i32 s82, s48, 2
	s_add_u32 s0, s46, 0x80
	s_addc_u32 s1, s47, 0
	s_cmp_eq_u32 s66, s48
	s_cselect_b32 s48, s2, s0
	s_cselect_b32 s49, s3, s1
	s_cselect_b32 s51, s45, s81
	s_cselect_b32 s50, s44, s80
	s_cmp_eq_u32 s99, 0
	s_cbranch_scc1 .Lkr5_a
	s_add_i32 m0, s56, 0xffffff80
	s_nop 0
	global_load_lds_dwordx4 v[192:193], off offset:128
	s_add_i32 m0, s57, 0xffffff80
	s_nop 0
	global_load_lds_dwordx4 v[194:195], off offset:128
.Lkr5_a:
	v_lshl_add_u64 v[192:193], s[46:47], 0, v[176:177]
	s_add_i32 m0, s10, 0xc000
	ds_read_b128 v[184:187], v199
	ds_read_b128 v[188:191], v199 offset:1024
	ds_read_b128 v[212:215], v199 offset:2048
	ds_read_b128 v[216:219], v199 offset:3072
	ds_read_b128 v[220:223], v199 offset:4096
	ds_read_b128 v[224:227], v199 offset:5120
	ds_read_b128 v[228:231], v199 offset:6144
	ds_read_b128 v[232:235], v199 offset:7168
	global_load_lds_dwordx4 v[192:193], off
	v_lshl_add_u64 v[192:193], s[46:47], 0, v[178:179]
	s_add_i32 m0, s10, 0xe000
	s_nop 0
	global_load_lds_dwordx4 v[192:193], off
	s_waitcnt vmcnt(8)
	s_waitcnt lgkmcnt(0)
	s_barrier
	s_setprio 1
	s_waitcnt lgkmcnt(0)
	v_mfma_scale_f32_16x16x128_f8f6f4 v[158:161], v[18:25], v[184:191], v[158:161], v200, v201 op_sel_hi:[0,0,0]
	v_mfma_scale_f32_16x16x128_f8f6f4 v[154:157], v[26:33], v[184:191], v[154:157], v200, v201 op_sel_hi:[0,0,0]
	v_mfma_scale_f32_16x16x128_f8f6f4 v[142:145], v[18:25], v[212:219], v[142:145], v200, v201 op_sel_hi:[0,0,0]
	v_mfma_scale_f32_16x16x128_f8f6f4 v[138:141], v[26:33], v[212:219], v[138:141], v200, v201 op_sel_hi:[0,0,0]
	v_mfma_scale_f32_16x16x128_f8f6f4 v[126:129], v[18:25], v[220:227], v[126:129], v200, v201 op_sel_hi:[0,0,0]
	v_mfma_scale_f32_16x16x128_f8f6f4 v[122:125], v[26:33], v[220:227], v[122:125], v200, v201 op_sel_hi:[0,0,0]
	v_mfma_scale_f32_16x16x128_f8f6f4 v[110:113], v[18:25], v[228:235], v[110:113], v200, v201 op_sel_hi:[0,0,0]
	v_mfma_scale_f32_16x16x128_f8f6f4 v[106:109], v[26:33], v[228:235], v[106:109], v200, v201 op_sel_hi:[0,0,0]
	s_setprio 0
	s_setprio 1
	v_mfma_scale_f32_16x16x128_f8f6f4 v[150:153], v[2:9], v[184:191], v[150:153], v200, v201 op_sel_hi:[0,0,0]
	v_mfma_scale_f32_16x16x128_f8f6f4 v[146:149], v[10:17], v[184:191], v[146:149], v200, v201 op_sel_hi:[0,0,0]
	v_mfma_scale_f32_16x16x128_f8f6f4 v[134:137], v[2:9], v[212:219], v[134:137], v200, v201 op_sel_hi:[0,0,0]
	v_mfma_scale_f32_16x16x128_f8f6f4 v[130:133], v[10:17], v[212:219], v[130:133], v200, v201 op_sel_hi:[0,0,0]
	v_mfma_scale_f32_16x16x128_f8f6f4 v[118:121], v[2:9], v[220:227], v[118:121], v200, v201 op_sel_hi:[0,0,0]
	v_mfma_scale_f32_16x16x128_f8f6f4 v[114:117], v[10:17], v[220:227], v[114:117], v200, v201 op_sel_hi:[0,0,0]
	v_mfma_scale_f32_16x16x128_f8f6f4 v[102:105], v[2:9], v[228:235], v[102:105], v200, v201 op_sel_hi:[0,0,0]
	v_mfma_scale_f32_16x16x128_f8f6f4 v[98:101], v[10:17], v[228:235], v[98:101], v200, v201 op_sel_hi:[0,0,0]
	s_setprio 0
	s_barrier
	s_add_i32 s0, s73, s9
	v_lshl_add_u64 v[184:185], s[50:51], 0, v[164:165]
	s_mov_b32 m0, s0
	ds_read_b128 v[212:215], v199 offset:16384
	ds_read_b128 v[216:219], v199 offset:17408
	ds_read_b128 v[220:223], v199 offset:18432
	ds_read_b128 v[224:227], v199 offset:19456
	ds_read_b128 v[228:231], v199 offset:20480
	ds_read_b128 v[232:235], v199 offset:21504
	ds_read_b128 v[236:239], v199 offset:22528
	ds_read_b128 v[240:243], v199 offset:23552
	global_load_lds_dwordx4 v[184:185], off
	s_add_i32 m0, s0, 0x2000
	s_add_u32 s0, s50, s14
	v_lshl_add_u64 v[186:187], s[50:51], 0, v[168:169]
	s_addc_u32 s1, s51, s15
	s_add_i32 s33, s74, s9
	global_load_lds_dwordx4 v[186:187], off
	v_lshl_add_u64 v[188:189], s[0:1], 0, v[164:165]
	s_mov_b32 m0, s33
	v_lshl_add_u64 v[190:191], s[0:1], 0, v[168:169]
	global_load_lds_dwordx4 v[188:189], off
	s_add_i32 m0, s33, 0x2000
	v_lshl_add_u64 v[192:193], s[48:49], 0, v[162:163]
	global_load_lds_dwordx4 v[190:191], off
	v_lshl_add_u64 v[194:195], s[48:49], 0, v[166:167]
	s_waitcnt vmcnt(6)
	s_waitcnt lgkmcnt(0)
	s_barrier
; #define PG8_STAGE(bufoff, gbase, voff) do { _Pragma("unroll") for (int _i = 0; _i < 2; ++_i) \
;         __builtin_amdgcn_global_load_lds((const unsigned*)((const char*)(gbase) + (voff)[_i]), (PG8_LAS unsigned*)(lds + (bufoff) + ldsw + _i * 8192), 16, 0, 0); } while (0)
; #define PG8_LDA(dst, b, h) do { _Pragma("unroll") for (int m = 0; m < 4; ++m) { const bf16x8 f0_ = *(const PG8_LAS bf16x8*)(lds + PG8_SA(b, h) + aoff + m * 2048), f1_ = *(const PG8_LAS bf16x8*)(lds + PG8_SA(b, h) + aoff + m * 2048 + 1024); dst[m].set(f0_, f1_); } } while (0)
; #define PG8_LDB(dst, b, h) do { _Pragma("unroll") for (int n = 0; n < 2; ++n) { const bf16x8 f0_ = *(const PG8_LAS bf16x8*)(lds + PG8_SB(b, h) + boff + n * 2048), f1_ = *(const PG8_LAS bf16x8*)(lds + PG8_SB(b, h) + boff + n * 2048 + 1024); dst[n].set(f0_, f1_); } } while (0)
; #define PG8_WAIT_V(n) asm volatile("s_waitcnt vmcnt(" #n ")" ::: "memory")
; #define PG8_WAIT_L(n) asm volatile("s_waitcnt lgkmcnt(" #n ")" ::: "memory")
; #define PG8_BAR __builtin_amdgcn_s_barrier()
; #define PG8_SCHED __builtin_amdgcn_sched_barrier(0)
; template <class Epi, class Sched, bool ALIGN_EPI = false, bool SP2 = false>
; __device__ __forceinline__ void gemm_phase(PG8_LAS unsigned char* lds, const Gemm g, const Sched& S, const Epi& E) {
;     ...
;             PG8_WAIT_V(8); PG8_WAIT_L(0); PG8_BAR; PG8_MMA(1, 0, At, B0); PG8_MMA(1, 1, At, B1); PG8_BAR; PG8_SCHED;
;             PG8_LDB(B0, 1, 0); PG8_LDB(B1, 1, 1); PG8_SCHED; PG8_LDA(At, 1, 0); PG8_STAGE(PG8_SA(0, 1), a2 + hstep, voffA);
;             PG8_WAIT_V(8); PG8_WAIT_L(0); PG8_BAR; PG8_MMA(0, 0, At, B0); PG8_MMA(0, 1, At, B1); PG8_BAR; PG8_SCHED;
;             PG8_LDA(At, 1, 1); PG8_STAGE(PG8_SB(1, 0), b3, voffB); PG8_STAGE(PG8_SB(1, 1), b3 + hstepB, voffB); PG8_STAGE(PG8_SA(1, 0), a3, voffA);
	s_setprio 1
	s_waitcnt lgkmcnt(0)
	v_mfma_scale_f32_16x16x128_f8f6f4 v[94:97], v[18:25], v[212:219], v[94:97], v200, v201 op_sel_hi:[0,0,0]
	v_mfma_scale_f32_16x16x128_f8f6f4 v[90:93], v[26:33], v[212:219], v[90:93], v200, v201 op_sel_hi:[0,0,0]
	v_mfma_scale_f32_16x16x128_f8f6f4 v[78:81], v[18:25], v[220:227], v[78:81], v200, v201 op_sel_hi:[0,0,0]
	v_mfma_scale_f32_16x16x128_f8f6f4 v[74:77], v[26:33], v[220:227], v[74:77], v200, v201 op_sel_hi:[0,0,0]
	v_mfma_scale_f32_16x16x128_f8f6f4 v[62:65], v[18:25], v[228:235], v[62:65], v200, v201 op_sel_hi:[0,0,0]
	v_mfma_scale_f32_16x16x128_f8f6f4 v[58:61], v[26:33], v[228:235], v[58:61], v200, v201 op_sel_hi:[0,0,0]
	v_mfma_scale_f32_16x16x128_f8f6f4 v[46:49], v[18:25], v[236:243], v[46:49], v200, v201 op_sel_hi:[0,0,0]
	v_mfma_scale_f32_16x16x128_f8f6f4 v[42:45], v[26:33], v[236:243], v[42:45], v200, v201 op_sel_hi:[0,0,0]
	s_setprio 0
	s_setprio 1
	v_mfma_scale_f32_16x16x128_f8f6f4 v[86:89], v[2:9], v[212:219], v[86:89], v200, v201 op_sel_hi:[0,0,0]
	v_mfma_scale_f32_16x16x128_f8f6f4 v[82:85], v[10:17], v[212:219], v[82:85], v200, v201 op_sel_hi:[0,0,0]
	v_mfma_scale_f32_16x16x128_f8f6f4 v[70:73], v[2:9], v[220:227], v[70:73], v200, v201 op_sel_hi:[0,0,0]
	v_mfma_scale_f32_16x16x128_f8f6f4 v[66:69], v[10:17], v[220:227], v[66:69], v200, v201 op_sel_hi:[0,0,0]
	v_mfma_scale_f32_16x16x128_f8f6f4 v[54:57], v[2:9], v[228:235], v[54:57], v200, v201 op_sel_hi:[0,0,0]
	v_mfma_scale_f32_16x16x128_f8f6f4 v[50:53], v[10:17], v[228:235], v[50:53], v200, v201 op_sel_hi:[0,0,0]
	v_mfma_scale_f32_16x16x128_f8f6f4 v[38:41], v[2:9], v[236:243], v[38:41], v200, v201 op_sel_hi:[0,0,0]
	v_mfma_scale_f32_16x16x128_f8f6f4 v[34:37], v[10:17], v[236:243], v[34:37], v200, v201 op_sel_hi:[0,0,0]
	s_setprio 0
	s_barrier
	s_add_i32 s33, 0, 0x18000
	s_add_i32 s50, 0, 0x1c000
	v_add_u32_e32 v14, s33, v173
	v_add_u32_e32 v30, s50, v173
	ds_read_b128 v[2:5], v14
	ds_read_b128 v[6:9], v14 offset:1024
	ds_read_b128 v[10:13], v14 offset:2048
	ds_read_b128 v[14:17], v14 offset:3072
	ds_read_b128 v[18:21], v30
	ds_read_b128 v[22:25], v30 offset:1024
	ds_read_b128 v[26:29], v30 offset:2048
	ds_read_b128 v[30:33], v30 offset:3072
	s_add_u32 s0, s48, s12
	s_addc_u32 s1, s49, s13
	s_mov_b32 m0, s52
	v_lshl_add_u64 v[204:205], s[0:1], 0, v[162:163]
	ds_read_b128 v[212:215], v199 offset:32768
	ds_read_b128 v[216:219], v199 offset:33792
	ds_read_b128 v[220:223], v199 offset:34816
	ds_read_b128 v[224:227], v199 offset:35840
	ds_read_b128 v[228:231], v199 offset:36864
	ds_read_b128 v[232:235], v199 offset:37888
	ds_read_b128 v[236:239], v199 offset:38912
	ds_read_b128 v[240:243], v199 offset:39936
	s_mov_b32 m0, s10
	s_nop 0
	global_load_lds_dwordx4 v[192:193], off
	s_mov_b32 m0, s11
	s_nop 0
	global_load_lds_dwordx4 v[194:195], off
	s_mov_b32 m0, s52
	s_nop 0
	global_load_lds_dwordx4 v[204:205], off
	v_lshl_add_u64 v[204:205], s[0:1], 0, v[166:167]
	s_mov_b32 m0, s53
	s_nop 0
	global_load_lds_dwordx4 v[204:205], off
	s_waitcnt vmcnt(8)
	s_waitcnt lgkmcnt(0)
	s_barrier
	s_setprio 1
	s_waitcnt lgkmcnt(0)
	v_mfma_scale_f32_16x16x128_f8f6f4 v[158:161], v[2:9], v[212:219], v[158:161], v200, v201 op_sel_hi:[0,0,0]
	v_mfma_scale_f32_16x16x128_f8f6f4 v[154:157], v[10:17], v[212:219], v[154:157], v200, v201 op_sel_hi:[0,0,0]
	v_mfma_scale_f32_16x16x128_f8f6f4 v[142:145], v[2:9], v[220:227], v[142:145], v200, v201 op_sel_hi:[0,0,0]
	v_mfma_scale_f32_16x16x128_f8f6f4 v[138:141], v[10:17], v[220:227], v[138:141], v200, v201 op_sel_hi:[0,0,0]
	v_mfma_scale_f32_16x16x128_f8f6f4 v[126:129], v[2:9], v[228:235], v[126:129], v200, v201 op_sel_hi:[0,0,0]
	v_mfma_scale_f32_16x16x128_f8f6f4 v[122:125], v[10:17], v[228:235], v[122:125], v200, v201 op_sel_hi:[0,0,0]
	v_mfma_scale_f32_16x16x128_f8f6f4 v[110:113], v[2:9], v[236:243], v[110:113], v200, v201 op_sel_hi:[0,0,0]
	v_mfma_scale_f32_16x16x128_f8f6f4 v[106:109], v[10:17], v[236:243], v[106:109], v200, v201 op_sel_hi:[0,0,0]
	s_setprio 0
	s_setprio 1
	v_mfma_scale_f32_16x16x128_f8f6f4 v[150:153], v[18:25], v[212:219], v[150:153], v200, v201 op_sel_hi:[0,0,0]
	v_mfma_scale_f32_16x16x128_f8f6f4 v[146:149], v[26:33], v[212:219], v[146:149], v200, v201 op_sel_hi:[0,0,0]
	v_mfma_scale_f32_16x16x128_f8f6f4 v[134:137], v[18:25], v[220:227], v[134:137], v200, v201 op_sel_hi:[0,0,0]
	v_mfma_scale_f32_16x16x128_f8f6f4 v[130:133], v[26:33], v[220:227], v[130:133], v200, v201 op_sel_hi:[0,0,0]
	v_mfma_scale_f32_16x16x128_f8f6f4 v[118:121], v[18:25], v[228:235], v[118:121], v200, v201 op_sel_hi:[0,0,0]
	v_mfma_scale_f32_16x16x128_f8f6f4 v[114:117], v[26:33], v[228:235], v[114:117], v200, v201 op_sel_hi:[0,0,0]
	v_mfma_scale_f32_16x16x128_f8f6f4 v[102:105], v[18:25], v[236:243], v[102:105], v200, v201 op_sel_hi:[0,0,0]
	v_mfma_scale_f32_16x16x128_f8f6f4 v[98:101], v[26:33], v[236:243], v[98:101], v200, v201 op_sel_hi:[0,0,0]
	s_setprio 0
	s_barrier
	s_add_i32 s0, s33, s9
	s_add_i32 m0, s0, 0xffffff80
	ds_read_b128 v[212:215], v199 offset:49152
	ds_read_b128 v[216:219], v199 offset:50176
	ds_read_b128 v[220:223], v199 offset:51200
	ds_read_b128 v[224:227], v199 offset:52224
	ds_read_b128 v[228:231], v199 offset:53248
	ds_read_b128 v[232:235], v199 offset:54272
	ds_read_b128 v[236:239], v199 offset:55296
	ds_read_b128 v[240:243], v199 offset:56320
	global_load_lds_dwordx4 v[184:185], off offset:128
	s_add_i32 m0, s0, 0x1f80
	s_add_i32 s0, s50, s9
	global_load_lds_dwordx4 v[186:187], off offset:128
	s_add_i32 m0, s0, 0xffffff80
	s_nop 0
	global_load_lds_dwordx4 v[188:189], off offset:128
	s_add_i32 m0, s0, 0x1f80
	s_nop 0
	global_load_lds_dwordx4 v[190:191], off offset:128
	s_cmp_ge_i32 s82, s58
	s_cbranch_scc0 .Lkr5_b
	s_add_i32 m0, s56, 0xffffff80
	s_nop 0
	global_load_lds_dwordx4 v[192:193], off offset:128
	s_add_i32 m0, s57, 0xffffff80
	s_nop 0
	global_load_lds_dwordx4 v[194:195], off offset:128

; #define PG8_STAGE(bufoff, gbase, voff) do { _Pragma("unroll") for (int _i = 0; _i < 2; ++_i) \
;         __builtin_amdgcn_global_load_lds((const unsigned*)((const char*)(gbase) + (voff)[_i]), (PG8_LAS unsigned*)(lds + (bufoff) + ldsw + _i * 8192), 16, 0, 0); } while (0)
; #define PG8_LDA(dst, b, h) do { _Pragma("unroll") for (int m = 0; m < 4; ++m) { const bf16x8 f0_ = *(const PG8_LAS bf16x8*)(lds + PG8_SA(b, h) + aoff + m * 2048), f1_ = *(const PG8_LAS bf16x8*)(lds + PG8_SA(b, h) + aoff + m * 2048 + 1024); dst[m].set(f0_, f1_); } } while (0)
; #define PG8_LDB(dst, b, h) do { _Pragma("unroll") for (int n = 0; n < 2; ++n) { const bf16x8 f0_ = *(const PG8_LAS bf16x8*)(lds + PG8_SB(b, h) + boff + n * 2048), f1_ = *(const PG8_LAS bf16x8*)(lds + PG8_SB(b, h) + boff + n * 2048 + 1024); dst[n].set(f0_, f1_); } } while (0)
; #define PG8_WAIT_V(n) asm volatile("s_waitcnt vmcnt(" #n ")" ::: "memory")
; #define PG8_WAIT_L(n) asm volatile("s_waitcnt lgkmcnt(" #n ")" ::: "memory")
; #define PG8_BAR __builtin_amdgcn_s_barrier()
; #define PG8_SCHED __builtin_amdgcn_sched_barrier(0)
; template <class Epi, class Sched, bool ALIGN_EPI = false, bool SP2 = false>
; __device__ __forceinline__ void gemm_phase(PG8_LAS unsigned char* lds, const Gemm g, const Sched& S, const Epi& E) {
;     ...
;             const bool last = (t == nt - 2);
;             const char* a1 = cA + (size_t)(t + 1) * kstep;
;             const char* a2 = last ? nA : cA + (size_t)(t + 2) * kstep; const char* b2 = last ? nB : cB + (size_t)(t + 2) * kstep;
;             const char* a3 = a2 + kstep; const char* b3 = b2 + kstep;
;             if (last && has_next) S.a_ready(nxt);
;             if constexpr (SP2) {
;             PG8_LDB(B0, 0, 0); PG8_LDB(B1, 0, 1); PG8_SCHED; PG8_LDA(At, 0, 0); PG8_STAGE(PG8_SA(1, 1), a1 + hstep, voffA);
;             PG8_WAIT_V(8); PG8_WAIT_L(0); PG8_BAR; PG8_MMA(0, 0, At, B0); PG8_MMA(0, 1, At, B1); PG8_BAR; PG8_SCHED;
;             PG8_LDA(At, 0, 1); PG8_STAGE(PG8_SB(0, 0), b2, voffB); PG8_STAGE(PG8_SB(0, 1), b2 + hstepB, voffB); PG8_STAGE(PG8_SA(0, 0), a2, voffA);
;             PG8_WAIT_V(8); PG8_WAIT_L(0); PG8_BAR; PG8_MMA(1, 0, At, B0); PG8_MMA(1, 1, At, B1); PG8_BAR; PG8_SCHED;
.LBB0_1658:
	ds_read_b128 v[16:19], v215
	ds_read_b128 v[20:23], v215 offset:1024
	ds_read_b128 v[24:27], v215 offset:2048
	ds_read_b128 v[28:31], v215 offset:3072
	ds_read_b128 v[0:3], v216
	ds_read_b128 v[4:7], v216 offset:1024
	ds_read_b128 v[8:11], v216 offset:2048
	ds_read_b128 v[12:15], v216 offset:3072
	s_add_i32 s83, s78, 2
	s_add_u32 s0, s2, 0x80
	s_addc_u32 s1, s3, 0
	s_cmp_eq_u32 s97, s78
	s_cselect_b32 s78, s58, s0
	s_cselect_b32 s79, s59, s1
	s_cselect_b32 s81, s75, s82
	s_cselect_b32 s80, s74, s57
	s_cmp_eq_u32 s99, 0
	s_cbranch_scc1 .Lkr6_a
	s_add_i32 m0, s93, 0xffffff80
	s_nop 0
	global_load_lds_dwordx4 v[168:169], off offset:128
	s_add_i32 m0, s94, 0xffffff80
	s_nop 0
	global_load_lds_dwordx4 v[170:171], off offset:128
.Lkr6_a:
	v_lshl_add_u64 v[206:207], s[2:3], 0, v[198:199]
	s_add_i32 m0, s71, 0xc000
	ds_read_b128 v[152:155], v217
	ds_read_b128 v[156:159], v217 offset:1024
	ds_read_b128 v[168:171], v217 offset:2048
	ds_read_b128 v[172:175], v217 offset:3072
	ds_read_b128 v[176:179], v217 offset:4096
	ds_read_b128 v[180:183], v217 offset:5120
	ds_read_b128 v[226:229], v217 offset:6144
	ds_read_b128 v[230:233], v217 offset:7168
	global_load_lds_dwordx4 v[206:207], off
	v_lshl_add_u64 v[206:207], s[2:3], 0, v[200:201]
	s_add_i32 m0, s71, 0xe000
	s_nop 0
	global_load_lds_dwordx4 v[206:207], off
	s_waitcnt vmcnt(8)
	s_waitcnt lgkmcnt(0)
	s_barrier
	s_setprio 1
	s_waitcnt lgkmcnt(0)
	v_mfma_scale_f32_16x16x128_f8f6f4 v[164:167], v[16:23], v[152:159], v[164:167], v218, v219 op_sel_hi:[0,0,0]
	v_mfma_scale_f32_16x16x128_f8f6f4 v[160:163], v[24:31], v[152:159], v[160:163], v218, v219 op_sel_hi:[0,0,0]
	v_mfma_scale_f32_16x16x128_f8f6f4 v[140:143], v[16:23], v[168:175], v[140:143], v218, v219 op_sel_hi:[0,0,0]
	v_mfma_scale_f32_16x16x128_f8f6f4 v[136:139], v[24:31], v[168:175], v[136:139], v218, v219 op_sel_hi:[0,0,0]
	v_mfma_scale_f32_16x16x128_f8f6f4 v[108:111], v[16:23], v[176:183], v[108:111], v218, v219 op_sel_hi:[0,0,0]
	v_mfma_scale_f32_16x16x128_f8f6f4 v[104:107], v[24:31], v[176:183], v[104:107], v218, v219 op_sel_hi:[0,0,0]
	v_mfma_scale_f32_16x16x128_f8f6f4 v[116:119], v[16:23], v[226:233], v[116:119], v218, v219 op_sel_hi:[0,0,0]
	v_mfma_scale_f32_16x16x128_f8f6f4 v[112:115], v[24:31], v[226:233], v[112:115], v218, v219 op_sel_hi:[0,0,0]
	s_setprio 0
	s_setprio 1
	v_mfma_scale_f32_16x16x128_f8f6f4 v[148:151], v[0:7], v[152:159], v[148:151], v218, v219 op_sel_hi:[0,0,0]
	v_mfma_scale_f32_16x16x128_f8f6f4 v[144:147], v[8:15], v[152:159], v[144:147], v218, v219 op_sel_hi:[0,0,0]
	v_mfma_scale_f32_16x16x128_f8f6f4 v[132:135], v[0:7], v[168:175], v[132:135], v218, v219 op_sel_hi:[0,0,0]
	v_mfma_scale_f32_16x16x128_f8f6f4 v[128:131], v[8:15], v[168:175], v[128:131], v218, v219 op_sel_hi:[0,0,0]
	v_mfma_scale_f32_16x16x128_f8f6f4 v[124:127], v[0:7], v[176:183], v[124:127], v218, v219 op_sel_hi:[0,0,0]
	v_mfma_scale_f32_16x16x128_f8f6f4 v[120:123], v[8:15], v[176:183], v[120:123], v218, v219 op_sel_hi:[0,0,0]
	v_mfma_scale_f32_16x16x128_f8f6f4 v[100:103], v[0:7], v[226:233], v[100:103], v218, v219 op_sel_hi:[0,0,0]
	v_mfma_scale_f32_16x16x128_f8f6f4 v[96:99], v[8:15], v[226:233], v[96:99], v218, v219 op_sel_hi:[0,0,0]
	s_setprio 0
	s_barrier
	s_add_i32 s0, s67, s45
	v_lshl_add_u64 v[152:153], s[80:81], 0, v[186:187]
	s_mov_b32 m0, s0
	ds_read_b128 v[172:175], v217 offset:16384
	ds_read_b128 v[176:179], v217 offset:17408
	ds_read_b128 v[226:229], v217 offset:18432
	ds_read_b128 v[230:233], v217 offset:19456
	ds_read_b128 v[234:237], v217 offset:20480
	ds_read_b128 v[238:241], v217 offset:21504
	ds_read_b128 v[242:245], v217 offset:22528
	ds_read_b128 v[246:249], v217 offset:23552
	global_load_lds_dwordx4 v[152:153], off
	s_add_i32 m0, s0, 0x2000
	s_add_u32 s0, s80, s20
	v_lshl_add_u64 v[154:155], s[80:81], 0, v[190:191]
	s_addc_u32 s1, s81, s21
	s_add_i32 s33, s10, s45
	global_load_lds_dwordx4 v[154:155], off
	v_lshl_add_u64 v[156:157], s[0:1], 0, v[186:187]
	s_mov_b32 m0, s33
	v_lshl_add_u64 v[158:159], s[0:1], 0, v[190:191]
	global_load_lds_dwordx4 v[156:157], off
	s_add_i32 m0, s33, 0x2000
	v_lshl_add_u64 v[168:169], s[78:79], 0, v[184:185]
	global_load_lds_dwordx4 v[158:159], off
	v_lshl_add_u64 v[170:171], s[78:79], 0, v[188:189]
	s_waitcnt vmcnt(6)
	s_waitcnt lgkmcnt(0)
	s_barrier
; #define PG8_STAGE(bufoff, gbase, voff) do { _Pragma("unroll") for (int _i = 0; _i < 2; ++_i) \
;         __builtin_amdgcn_global_load_lds((const unsigned*)((const char*)(gbase) + (voff)[_i]), (PG8_LAS unsigned*)(lds + (bufoff) + ldsw + _i * 8192), 16, 0, 0); } while (0)
; #define PG8_LDA(dst, b, h) do { _Pragma("unroll") for (int m = 0; m < 4; ++m) { const bf16x8 f0_ = *(const PG8_LAS bf16x8*)(lds + PG8_SA(b, h) + aoff + m * 2048), f1_ = *(const PG8_LAS bf16x8*)(lds + PG8_SA(b, h) + aoff + m * 2048 + 1024); dst[m].set(f0_, f1_); } } while (0)
; #define PG8_LDB(dst, b, h) do { _Pragma("unroll") for (int n = 0; n < 2; ++n) { const bf16x8 f0_ = *(const PG8_LAS bf16x8*)(lds + PG8_SB(b, h) + boff + n * 2048), f1_ = *(const PG8_LAS bf16x8*)(lds + PG8_SB(b, h) + boff + n * 2048 + 1024); dst[n].set(f0_, f1_); } } while (0)
; #define PG8_WAIT_V(n) asm volatile("s_waitcnt vmcnt(" #n ")" ::: "memory")
; #define PG8_WAIT_L(n) asm volatile("s_waitcnt lgkmcnt(" #n ")" ::: "memory")
; #define PG8_BAR __builtin_amdgcn_s_barrier()
; #define PG8_SCHED __builtin_amdgcn_sched_barrier(0)
; template <class Epi, class Sched, bool ALIGN_EPI = false, bool SP2 = false>
; __device__ __forceinline__ void gemm_phase(PG8_LAS unsigned char* lds, const Gemm g, const Sched& S, const Epi& E) {
;     ...
;             PG8_WAIT_V(8); PG8_WAIT_L(0); PG8_BAR; PG8_MMA(1, 0, At, B0); PG8_MMA(1, 1, At, B1); PG8_BAR; PG8_SCHED;
;             PG8_LDB(B0, 1, 0); PG8_LDB(B1, 1, 1); PG8_SCHED; PG8_LDA(At, 1, 0); PG8_STAGE(PG8_SA(0, 1), a2 + hstep, voffA);
;             PG8_WAIT_V(8); PG8_WAIT_L(0); PG8_BAR; PG8_MMA(0, 0, At, B0); PG8_MMA(0, 1, At, B1); PG8_BAR; PG8_SCHED;
;             PG8_LDA(At, 1, 1); PG8_STAGE(PG8_SB(1, 0), b3, voffB); PG8_STAGE(PG8_SB(1, 1), b3 + hstepB, voffB); PG8_STAGE(PG8_SA(1, 0), a3, voffA);
	s_setprio 1
	s_waitcnt lgkmcnt(0)
	v_mfma_scale_f32_16x16x128_f8f6f4 v[92:95], v[16:23], v[172:179], v[92:95], v218, v219 op_sel_hi:[0,0,0]
	v_mfma_scale_f32_16x16x128_f8f6f4 v[88:91], v[24:31], v[172:179], v[88:91], v218, v219 op_sel_hi:[0,0,0]
	v_mfma_scale_f32_16x16x128_f8f6f4 v[76:79], v[16:23], v[226:233], v[76:79], v218, v219 op_sel_hi:[0,0,0]
	v_mfma_scale_f32_16x16x128_f8f6f4 v[72:75], v[24:31], v[226:233], v[72:75], v218, v219 op_sel_hi:[0,0,0]
	v_mfma_scale_f32_16x16x128_f8f6f4 v[60:63], v[16:23], v[234:241], v[60:63], v218, v219 op_sel_hi:[0,0,0]
	v_mfma_scale_f32_16x16x128_f8f6f4 v[56:59], v[24:31], v[234:241], v[56:59], v218, v219 op_sel_hi:[0,0,0]
	v_mfma_scale_f32_16x16x128_f8f6f4 v[44:47], v[16:23], v[242:249], v[44:47], v218, v219 op_sel_hi:[0,0,0]
	v_mfma_scale_f32_16x16x128_f8f6f4 v[40:43], v[24:31], v[242:249], v[40:43], v218, v219 op_sel_hi:[0,0,0]
	s_setprio 0
	s_setprio 1
	v_mfma_scale_f32_16x16x128_f8f6f4 v[84:87], v[0:7], v[172:179], v[84:87], v218, v219 op_sel_hi:[0,0,0]
	v_mfma_scale_f32_16x16x128_f8f6f4 v[80:83], v[8:15], v[172:179], v[80:83], v218, v219 op_sel_hi:[0,0,0]
	v_mfma_scale_f32_16x16x128_f8f6f4 v[68:71], v[0:7], v[226:233], v[68:71], v218, v219 op_sel_hi:[0,0,0]
	v_mfma_scale_f32_16x16x128_f8f6f4 v[64:67], v[8:15], v[226:233], v[64:67], v218, v219 op_sel_hi:[0,0,0]
	v_mfma_scale_f32_16x16x128_f8f6f4 v[52:55], v[0:7], v[234:241], v[52:55], v218, v219 op_sel_hi:[0,0,0]
	v_mfma_scale_f32_16x16x128_f8f6f4 v[48:51], v[8:15], v[234:241], v[48:51], v218, v219 op_sel_hi:[0,0,0]
	v_mfma_scale_f32_16x16x128_f8f6f4 v[36:39], v[0:7], v[242:249], v[36:39], v218, v219 op_sel_hi:[0,0,0]
	v_mfma_scale_f32_16x16x128_f8f6f4 v[32:35], v[8:15], v[242:249], v[32:35], v218, v219 op_sel_hi:[0,0,0]
	s_setprio 0
	s_barrier
	s_add_i32 s33, 0, 0x18000
	s_add_i32 s80, 0, 0x1c000
	v_add_u32_e32 v12, s33, v211
	v_add_u32_e32 v28, s80, v211
	ds_read_b128 v[0:3], v12
	ds_read_b128 v[4:7], v12 offset:1024
	ds_read_b128 v[8:11], v12 offset:2048
	ds_read_b128 v[12:15], v12 offset:3072
	ds_read_b128 v[16:19], v28
	ds_read_b128 v[20:23], v28 offset:1024
	ds_read_b128 v[24:27], v28 offset:2048
	ds_read_b128 v[28:31], v28 offset:3072
	s_add_u32 s0, s78, s18
	s_addc_u32 s1, s79, s19
	s_mov_b32 m0, s86
	v_lshl_add_u64 v[180:181], s[0:1], 0, v[184:185]
	ds_read_b128 v[172:175], v217 offset:32768
	ds_read_b128 v[176:179], v217 offset:33792
	ds_read_b128 v[226:229], v217 offset:34816
	ds_read_b128 v[230:233], v217 offset:35840
	ds_read_b128 v[234:237], v217 offset:36864
	ds_read_b128 v[238:241], v217 offset:37888
	ds_read_b128 v[242:245], v217 offset:38912
	ds_read_b128 v[246:249], v217 offset:39936
	s_mov_b32 m0, s71
	s_nop 0
	global_load_lds_dwordx4 v[168:169], off
	s_mov_b32 m0, s73
	s_nop 0
	global_load_lds_dwordx4 v[170:171], off
	s_mov_b32 m0, s86
	s_nop 0
	global_load_lds_dwordx4 v[180:181], off
	v_lshl_add_u64 v[180:181], s[0:1], 0, v[188:189]
	s_mov_b32 m0, s87
	s_nop 0
	global_load_lds_dwordx4 v[180:181], off
	s_waitcnt vmcnt(8)
	s_waitcnt lgkmcnt(0)
	s_barrier
	s_setprio 1
	s_waitcnt lgkmcnt(0)
	v_mfma_scale_f32_16x16x128_f8f6f4 v[164:167], v[0:7], v[172:179], v[164:167], v218, v219 op_sel_hi:[0,0,0]
	v_mfma_scale_f32_16x16x128_f8f6f4 v[160:163], v[8:15], v[172:179], v[160:163], v218, v219 op_sel_hi:[0,0,0]
	v_mfma_scale_f32_16x16x128_f8f6f4 v[140:143], v[0:7], v[226:233], v[140:143], v218, v219 op_sel_hi:[0,0,0]
	v_mfma_scale_f32_16x16x128_f8f6f4 v[136:139], v[8:15], v[226:233], v[136:139], v218, v219 op_sel_hi:[0,0,0]
	v_mfma_scale_f32_16x16x128_f8f6f4 v[108:111], v[0:7], v[234:241], v[108:111], v218, v219 op_sel_hi:[0,0,0]
	v_mfma_scale_f32_16x16x128_f8f6f4 v[104:107], v[8:15], v[234:241], v[104:107], v218, v219 op_sel_hi:[0,0,0]
	v_mfma_scale_f32_16x16x128_f8f6f4 v[116:119], v[0:7], v[242:249], v[116:119], v218, v219 op_sel_hi:[0,0,0]
	v_mfma_scale_f32_16x16x128_f8f6f4 v[112:115], v[8:15], v[242:249], v[112:115], v218, v219 op_sel_hi:[0,0,0]
	s_setprio 0
	s_setprio 1
	v_mfma_scale_f32_16x16x128_f8f6f4 v[148:151], v[16:23], v[172:179], v[148:151], v218, v219 op_sel_hi:[0,0,0]
	v_mfma_scale_f32_16x16x128_f8f6f4 v[144:147], v[24:31], v[172:179], v[144:147], v218, v219 op_sel_hi:[0,0,0]
	v_mfma_scale_f32_16x16x128_f8f6f4 v[132:135], v[16:23], v[226:233], v[132:135], v218, v219 op_sel_hi:[0,0,0]
	v_mfma_scale_f32_16x16x128_f8f6f4 v[128:131], v[24:31], v[226:233], v[128:131], v218, v219 op_sel_hi:[0,0,0]
	v_mfma_scale_f32_16x16x128_f8f6f4 v[124:127], v[16:23], v[234:241], v[124:127], v218, v219 op_sel_hi:[0,0,0]
	v_mfma_scale_f32_16x16x128_f8f6f4 v[120:123], v[24:31], v[234:241], v[120:123], v218, v219 op_sel_hi:[0,0,0]
	v_mfma_scale_f32_16x16x128_f8f6f4 v[100:103], v[16:23], v[242:249], v[100:103], v218, v219 op_sel_hi:[0,0,0]
	v_mfma_scale_f32_16x16x128_f8f6f4 v[96:99], v[24:31], v[242:249], v[96:99], v218, v219 op_sel_hi:[0,0,0]
	s_setprio 0
	s_barrier
	s_add_i32 s0, s33, s45
	s_add_i32 m0, s0, 0xffffff80
	ds_read_b128 v[172:175], v217 offset:49152
	ds_read_b128 v[176:179], v217 offset:50176
	ds_read_b128 v[226:229], v217 offset:51200
	ds_read_b128 v[230:233], v217 offset:52224
	ds_read_b128 v[234:237], v217 offset:53248
	ds_read_b128 v[238:241], v217 offset:54272
	ds_read_b128 v[242:245], v217 offset:55296
	ds_read_b128 v[246:249], v217 offset:56320
	global_load_lds_dwordx4 v[152:153], off offset:128
	s_add_i32 m0, s0, 0x1f80
	s_add_i32 s0, s80, s45
	global_load_lds_dwordx4 v[154:155], off offset:128
	s_add_i32 m0, s0, 0xffffff80
	s_nop 0
	global_load_lds_dwordx4 v[156:157], off offset:128
	s_add_i32 m0, s0, 0x1f80
	s_nop 0
	global_load_lds_dwordx4 v[158:159], off offset:128
	s_cmp_ge_i32 s83, s91
	s_cbranch_scc0 .Lkr6_b
	s_add_i32 m0, s93, 0xffffff80
	s_nop 0
	global_load_lds_dwordx4 v[168:169], off offset:128
	s_add_i32 m0, s94, 0xffffff80
	s_nop 0
	global_load_lds_dwordx4 v[170:171], off offset:128
